# stack7 + gate/up and down: leading half's pre-epilogue barrier moved after its first two epilogue row groups (runs beside the partner's last MFMA block)
# baseline (speedup 1.0000x reference)
.LBB0_1546:
	v_lshlrev_b32_e32 v150, 16, v86
	v_and_b32_e32 v151, 0xffff0000, v86
	v_mul_f32_e32 v158, 0x3d800000, v177
	v_pk_fma_f32 v[130:131], v[158:159], v[130:131], v[150:151] op_sel_hi:[0,1,1]
	v_min_f32_e32 v130, 0x41898193, v130
	v_min_f32_e32 v131, 0x41898193, v131
	v_exp_f32_e64 v178, -v130
	v_exp_f32_e64 v179, -v131
	v_lshlrev_b32_e32 v156, 16, v87
	v_and_b32_e32 v157, 0xffff0000, v87
	v_lshlrev_b32_e32 v152, 16, v82
	v_pk_add_f32 v[178:179], v[178:179], 1.0 op_sel_hi:[1,0]
	v_and_b32_e32 v153, 0xffff0000, v82
	v_rcp_f32_e32 v178, v178
	v_rcp_f32_e32 v179, v179
	v_lshlrev_b32_e32 v154, 16, v83
	v_and_b32_e32 v155, 0xffff0000, v83
	v_pk_fma_f32 v[132:133], v[158:159], v[132:133], v[156:157] op_sel_hi:[0,1,1]
	v_pk_fma_f32 v[134:135], v[158:159], v[134:135], v[152:153] op_sel_hi:[0,1,1]
	v_pk_fma_f32 v[136:137], v[158:159], v[136:137], v[154:155] op_sel_hi:[0,1,1]
	v_med3_f32 v134, v134, s70, v167
	v_med3_f32 v135, v135, s70, v167
	v_pk_mul_f32 v[130:131], v[130:131], v[178:179]
	v_min_f32_e32 v132, 0x41898193, v132
	v_min_f32_e32 v133, 0x41898193, v133
	v_pk_mul_f32 v[130:131], v[130:131], v[134:135]
	v_med3_f32 v134, v136, s70, v167
	v_med3_f32 v135, v137, s70, v167
	v_exp_f32_e64 v136, -v132
	v_exp_f32_e64 v137, -v133
	v_lshlrev_b32_e32 v86, 16, v88
	v_and_b32_e32 v87, 0xffff0000, v88
	v_pk_fma_f32 v[122:123], v[158:159], v[122:123], v[86:87] op_sel_hi:[0,1,1]
	v_pk_add_f32 v[136:137], v[136:137], 1.0 op_sel_hi:[1,0]
	v_min_f32_e32 v122, 0x41898193, v122
	v_rcp_f32_e32 v136, v136
	v_rcp_f32_e32 v137, v137
	v_min_f32_e32 v123, 0x41898193, v123
	v_lshlrev_b32_e32 v88, 16, v89
	v_and_b32_e32 v89, 0xffff0000, v89
	v_pk_mul_f32 v[132:133], v[132:133], v[136:137]
	v_lshlrev_b32_e32 v82, 16, v84
	v_pk_mul_f32 v[132:133], v[132:133], v[134:135]
	v_exp_f32_e64 v134, -v122
	v_exp_f32_e64 v135, -v123
	v_and_b32_e32 v83, 0xffff0000, v84
	v_lshlrev_b32_e32 v84, 16, v85
	v_and_b32_e32 v85, 0xffff0000, v85
	v_pk_add_f32 v[134:135], v[134:135], 1.0 op_sel_hi:[1,0]
	v_pk_fma_f32 v[124:125], v[158:159], v[124:125], v[88:89] op_sel_hi:[0,1,1]
	v_rcp_f32_e32 v134, v134
	v_rcp_f32_e32 v135, v135
	v_pk_fma_f32 v[126:127], v[158:159], v[126:127], v[82:83] op_sel_hi:[0,1,1]
	v_pk_fma_f32 v[128:129], v[158:159], v[128:129], v[84:85] op_sel_hi:[0,1,1]
	v_med3_f32 v126, v126, s70, v167
	v_med3_f32 v127, v127, s70, v167
	v_pk_mul_f32 v[122:123], v[122:123], v[134:135]
	v_min_f32_e32 v124, 0x41898193, v124
	v_min_f32_e32 v125, 0x41898193, v125
	v_pk_mul_f32 v[122:123], v[122:123], v[126:127]
	v_med3_f32 v126, v128, s70, v167
	v_med3_f32 v127, v129, s70, v167
	v_exp_f32_e64 v128, -v124
	v_exp_f32_e64 v129, -v125
	v_mov_b32_e32 v142, v0
	s_and_b64 vcc, exec, s[6:7]
	v_pk_add_f32 v[128:129], v[128:129], 1.0 op_sel_hi:[1,0]
	v_readfirstlane_b32 s69, v142
	v_rcp_f32_e32 v128, v128
	v_rcp_f32_e32 v129, v129
	s_ashr_i32 s8, s69, 6
	s_mul_i32 s9, s8, 0xb00
	s_add_i32 s71, s9, 0
	v_pk_mul_f32 v[124:125], v[124:125], v[128:129]
	v_and_b32_e32 v147, 15, v142
	v_pk_mul_f32 v[124:125], v[124:125], v[126:127]
	v_mov_b32_e32 v126, 0
	v_mov_b32_e32 v127, 0
	v_cvt_pk_fp8_f32 v126, v130, v131
	v_cvt_pk_fp8_f32 v127, v122, v123
	v_lshrrev_b32_e32 v123, 1, v142
	s_add_i32 s71, s71, 0x20000
	v_cvt_pk_fp8_f32 v126, v132, v133 op_sel:[0,0,1]
	v_cvt_pk_fp8_f32 v127, v124, v125 op_sel:[0,0,1]
	v_mul_f32_e32 v124, 0x3d800000, v176
	v_mul_u32_u24_e32 v122, 48, v147
	v_and_b32_e32 v123, 24, v123
	v_pk_fma_f32 v[114:115], v[124:125], v[114:115], v[150:151] op_sel_hi:[0,1,1]
	v_add3_u32 v122, s71, v122, v123
	v_min_f32_e32 v114, 0x41898193, v114
	v_min_f32_e32 v115, 0x41898193, v115
	ds_write_b64 v122, v[126:127]
	v_exp_f32_e64 v126, -v114
	v_exp_f32_e64 v127, -v115
	v_pk_fma_f32 v[116:117], v[124:125], v[116:117], v[156:157] op_sel_hi:[0,1,1]
	v_pk_fma_f32 v[118:119], v[124:125], v[118:119], v[152:153] op_sel_hi:[0,1,1]
	v_pk_fma_f32 v[120:121], v[124:125], v[120:121], v[154:155] op_sel_hi:[0,1,1]
	v_pk_add_f32 v[126:127], v[126:127], 1.0 op_sel_hi:[1,0]
	v_med3_f32 v118, v118, s70, v167
	v_rcp_f32_e32 v126, v126
	v_rcp_f32_e32 v127, v127
	v_med3_f32 v119, v119, s70, v167
	v_min_f32_e32 v116, 0x41898193, v116
	v_min_f32_e32 v117, 0x41898193, v117
	v_pk_mul_f32 v[114:115], v[114:115], v[126:127]
	v_pk_fma_f32 v[106:107], v[124:125], v[106:107], v[86:87] op_sel_hi:[0,1,1]
	v_pk_mul_f32 v[114:115], v[114:115], v[118:119]
	v_med3_f32 v118, v120, s70, v167
	v_med3_f32 v119, v121, s70, v167
	v_exp_f32_e64 v120, -v116
	v_exp_f32_e64 v121, -v117
	v_min_f32_e32 v106, 0x41898193, v106
	v_min_f32_e32 v107, 0x41898193, v107
	v_pk_fma_f32 v[108:109], v[124:125], v[108:109], v[88:89] op_sel_hi:[0,1,1]
	v_pk_add_f32 v[120:121], v[120:121], 1.0 op_sel_hi:[1,0]
	v_pk_fma_f32 v[110:111], v[124:125], v[110:111], v[82:83] op_sel_hi:[0,1,1]
	v_rcp_f32_e32 v120, v120
	v_rcp_f32_e32 v121, v121
	v_pk_fma_f32 v[112:113], v[124:125], v[112:113], v[84:85] op_sel_hi:[0,1,1]
	v_med3_f32 v110, v110, s70, v167
	v_med3_f32 v111, v111, s70, v167
	v_pk_mul_f32 v[116:117], v[116:117], v[120:121]
	v_min_f32_e32 v108, 0x41898193, v108
	v_pk_mul_f32 v[116:117], v[116:117], v[118:119]
	v_exp_f32_e64 v118, -v106
	v_exp_f32_e64 v119, -v107
	v_min_f32_e32 v109, 0x41898193, v109
	s_ashr_i32 s69, s69, 2
	s_andn2_b32 s69, s69, 63
	v_pk_add_f32 v[118:119], v[118:119], 1.0 op_sel_hi:[1,0]
	s_lshl_b32 s8, s8, 5
	v_rcp_f32_e32 v118, v118
	v_rcp_f32_e32 v119, v119
	s_lshl_b32 s9, s80, 7
	s_and_b32 s8, s8, 0x60
	s_or_b32 s8, s8, s9
	v_pk_mul_f32 v[106:107], v[106:107], v[118:119]
	s_ashr_i32 s9, s8, 31
	v_pk_mul_f32 v[106:107], v[106:107], v[110:111]
	v_med3_f32 v110, v112, s70, v167
	v_med3_f32 v111, v113, s70, v167
	v_exp_f32_e64 v112, -v108
	v_exp_f32_e64 v113, -v109
	s_nop 0
	v_pk_add_f32 v[112:113], v[112:113], 1.0 op_sel_hi:[1,0]
	s_nop 0
	v_rcp_f32_e32 v112, v112
	v_rcp_f32_e32 v113, v113
	s_nop 0
	v_pk_mul_f32 v[108:109], v[108:109], v[112:113]
	s_nop 0
	v_pk_mul_f32 v[108:109], v[108:109], v[110:111]
	v_mov_b32_e32 v110, 0
	v_mov_b32_e32 v111, 0
	v_cvt_pk_fp8_f32 v110, v114, v115
	v_cvt_pk_fp8_f32 v111, v106, v107
	v_bfe_u32 v106, v142, 1, 5
	v_mul_u32_u24_e32 v107, 48, v106
	v_cvt_pk_fp8_f32 v110, v116, v117 op_sel:[0,0,1]
	v_cvt_pk_fp8_f32 v111, v108, v109 op_sel:[0,0,1]
	v_lshlrev_b32_e32 v108, 4, v142
	v_and_b32_e32 v142, 16, v108
	v_lshl_or_b32 v106, s78, 8, v106
	ds_write_b64 v122, v[110:111] offset:768
	v_add3_u32 v108, s71, v107, v142
	v_add_u32_e32 v106, s69, v106
	ds_read_b128 v[110:113], v108
	v_ashrrev_i32_e32 v107, 31, v106
	v_lshlrev_b64 v[114:115], 10, v[106:107]
	v_lshl_add_u64 v[114:115], s[16:17], 0, v[114:115]
	v_lshl_add_u64 v[114:115], v[114:115], 0, s[8:9]
	v_lshl_add_u64 v[114:115], v[114:115], 0, v[142:143]
	s_waitcnt lgkmcnt(0)
	global_store_dwordx4 v[114:115], v[110:113], off
	s_cmp_lg_u64 s[26:27], 0
	s_cbranch_scc0 .Lepibar_gu0
	s_barrier
.Lepibar_gu0:
	s_nop 1
	v_mul_f32_e32 v110, 0x3d800000, v175
	v_pk_fma_f32 v[98:99], v[110:111], v[98:99], v[150:151] op_sel_hi:[0,1,1]
	v_min_f32_e32 v98, 0x41898193, v98
	v_min_f32_e32 v99, 0x41898193, v99
	v_exp_f32_e64 v112, -v98
	v_exp_f32_e64 v113, -v99
	v_pk_fma_f32 v[100:101], v[110:111], v[100:101], v[156:157] op_sel_hi:[0,1,1]
	v_pk_fma_f32 v[102:103], v[110:111], v[102:103], v[152:153] op_sel_hi:[0,1,1]
	v_pk_fma_f32 v[104:105], v[110:111], v[104:105], v[154:155] op_sel_hi:[0,1,1]
	v_pk_add_f32 v[112:113], v[112:113], 1.0 op_sel_hi:[1,0]
	v_med3_f32 v102, v102, s70, v167
	v_rcp_f32_e32 v112, v112
	v_rcp_f32_e32 v113, v113
	v_med3_f32 v103, v103, s70, v167
	v_min_f32_e32 v100, 0x41898193, v100
	v_min_f32_e32 v101, 0x41898193, v101
	v_pk_mul_f32 v[98:99], v[98:99], v[112:113]
	v_pk_fma_f32 v[90:91], v[110:111], v[90:91], v[86:87] op_sel_hi:[0,1,1]
	v_pk_mul_f32 v[98:99], v[98:99], v[102:103]
	v_med3_f32 v102, v104, s70, v167
	v_med3_f32 v103, v105, s70, v167
	v_exp_f32_e64 v104, -v100
	v_exp_f32_e64 v105, -v101
	v_min_f32_e32 v90, 0x41898193, v90
	v_min_f32_e32 v91, 0x41898193, v91
	v_pk_fma_f32 v[92:93], v[110:111], v[92:93], v[88:89] op_sel_hi:[0,1,1]
	v_pk_add_f32 v[104:105], v[104:105], 1.0 op_sel_hi:[1,0]
	v_pk_fma_f32 v[94:95], v[110:111], v[94:95], v[82:83] op_sel_hi:[0,1,1]
	v_rcp_f32_e32 v104, v104
	v_rcp_f32_e32 v105, v105
	v_pk_fma_f32 v[96:97], v[110:111], v[96:97], v[84:85] op_sel_hi:[0,1,1]
	v_med3_f32 v94, v94, s70, v167
	v_med3_f32 v95, v95, s70, v167
	v_pk_mul_f32 v[100:101], v[100:101], v[104:105]
	v_min_f32_e32 v92, 0x41898193, v92
	v_pk_mul_f32 v[100:101], v[100:101], v[102:103]
	v_exp_f32_e64 v102, -v90
	v_exp_f32_e64 v103, -v91
	v_min_f32_e32 v93, 0x41898193, v93
	v_pk_add_f32 v[102:103], v[102:103], 1.0 op_sel_hi:[1,0]
	s_nop 0
	v_rcp_f32_e32 v102, v102
	v_rcp_f32_e32 v103, v103
	s_nop 0
	v_pk_mul_f32 v[90:91], v[90:91], v[102:103]
	s_nop 0
	v_pk_mul_f32 v[90:91], v[90:91], v[94:95]
	v_med3_f32 v94, v96, s70, v167
	v_med3_f32 v95, v97, s70, v167
	v_exp_f32_e64 v96, -v92
	v_exp_f32_e64 v97, -v93
	s_nop 0
	v_pk_add_f32 v[96:97], v[96:97], 1.0 op_sel_hi:[1,0]
	s_nop 0
	v_rcp_f32_e32 v96, v96
	v_rcp_f32_e32 v97, v97
	s_nop 0
	v_pk_mul_f32 v[92:93], v[92:93], v[96:97]
	s_nop 0
	v_pk_mul_f32 v[92:93], v[92:93], v[94:95]
	v_mov_b32_e32 v95, v143
	v_cvt_pk_fp8_f32 v95, v90, v91
	v_mul_f32_e32 v90, 0x3d800000, v174
	v_pk_fma_f32 v[74:75], v[90:91], v[74:75], v[150:151] op_sel_hi:[0,1,1]
	v_min_f32_e32 v74, 0x41898193, v74
	v_min_f32_e32 v75, 0x41898193, v75
	v_cvt_pk_fp8_f32 v95, v92, v93 op_sel:[0,0,1]
	v_exp_f32_e64 v92, -v74
	v_exp_f32_e64 v93, -v75
	v_pk_fma_f32 v[76:77], v[90:91], v[76:77], v[156:157] op_sel_hi:[0,1,1]
	v_pk_fma_f32 v[78:79], v[90:91], v[78:79], v[152:153] op_sel_hi:[0,1,1]
	v_pk_fma_f32 v[80:81], v[90:91], v[80:81], v[154:155] op_sel_hi:[0,1,1]
	v_pk_add_f32 v[92:93], v[92:93], 1.0 op_sel_hi:[1,0]
	v_med3_f32 v78, v78, s70, v167
	v_rcp_f32_e32 v92, v92
	v_rcp_f32_e32 v93, v93
	v_med3_f32 v79, v79, s70, v167
	v_min_f32_e32 v76, 0x41898193, v76
	v_min_f32_e32 v77, 0x41898193, v77
	v_pk_mul_f32 v[74:75], v[74:75], v[92:93]
	v_pk_fma_f32 v[66:67], v[90:91], v[66:67], v[86:87] op_sel_hi:[0,1,1]
	v_pk_mul_f32 v[74:75], v[74:75], v[78:79]
	v_med3_f32 v78, v80, s70, v167
	v_med3_f32 v79, v81, s70, v167
	v_exp_f32_e64 v80, -v76
	v_exp_f32_e64 v81, -v77
	v_min_f32_e32 v66, 0x41898193, v66
	v_min_f32_e32 v67, 0x41898193, v67
	v_pk_fma_f32 v[68:69], v[90:91], v[68:69], v[88:89] op_sel_hi:[0,1,1]
	v_pk_add_f32 v[80:81], v[80:81], 1.0 op_sel_hi:[1,0]
	v_pk_fma_f32 v[70:71], v[90:91], v[70:71], v[82:83] op_sel_hi:[0,1,1]
	v_rcp_f32_e32 v80, v80
	v_rcp_f32_e32 v81, v81
	v_pk_fma_f32 v[72:73], v[90:91], v[72:73], v[84:85] op_sel_hi:[0,1,1]
	v_med3_f32 v70, v70, s70, v167
	v_med3_f32 v71, v71, s70, v167
	v_pk_mul_f32 v[76:77], v[76:77], v[80:81]
	v_min_f32_e32 v68, 0x41898193, v68
	v_pk_mul_f32 v[76:77], v[76:77], v[78:79]
	v_exp_f32_e64 v78, -v66
	v_exp_f32_e64 v79, -v67
	v_min_f32_e32 v69, 0x41898193, v69
	v_mov_b32_e32 v94, v143
	v_cvt_pk_fp8_f32 v94, v98, v99
	v_pk_add_f32 v[78:79], v[78:79], 1.0 op_sel_hi:[1,0]
	v_cvt_pk_fp8_f32 v94, v100, v101 op_sel:[0,0,1]
	v_rcp_f32_e32 v78, v78
	v_rcp_f32_e32 v79, v79
	ds_write_b64 v122, v[94:95]
	v_pk_mul_f32 v[66:67], v[66:67], v[78:79]
	s_nop 0
	v_pk_mul_f32 v[66:67], v[66:67], v[70:71]
	v_med3_f32 v70, v72, s70, v167
	v_med3_f32 v71, v73, s70, v167
	v_exp_f32_e64 v72, -v68
	v_exp_f32_e64 v73, -v69
	s_nop 0
	v_pk_add_f32 v[72:73], v[72:73], 1.0 op_sel_hi:[1,0]
	s_nop 0
	v_rcp_f32_e32 v72, v72
	v_rcp_f32_e32 v73, v73
	s_nop 0
	v_pk_mul_f32 v[68:69], v[68:69], v[72:73]
	s_nop 0
	v_pk_mul_f32 v[68:69], v[68:69], v[70:71]
	v_mov_b32_e32 v70, v143
	v_mov_b32_e32 v71, v143
	v_cvt_pk_fp8_f32 v70, v74, v75
	v_cvt_pk_fp8_f32 v71, v66, v67
	v_cvt_pk_fp8_f32 v70, v76, v77 op_sel:[0,0,1]
	v_cvt_pk_fp8_f32 v71, v68, v69 op_sel:[0,0,1]
	ds_write_b64 v122, v[70:71] offset:768
	v_or_b32_e32 v70, 32, v106
	ds_read_b128 v[66:69], v108
	v_ashrrev_i32_e32 v71, 31, v70
	v_lshlrev_b64 v[70:71], 10, v[70:71]
	v_lshl_add_u64 v[70:71], s[16:17], 0, v[70:71]
	v_lshl_add_u64 v[70:71], v[70:71], 0, s[8:9]
	v_lshl_add_u64 v[70:71], v[70:71], 0, v[142:143]
	s_waitcnt lgkmcnt(0)
	global_store_dwordx4 v[70:71], v[66:69], off
	s_nop 1
	v_mul_f32_e32 v66, 0x3d800000, v173
	v_pk_fma_f32 v[58:59], v[66:67], v[58:59], v[150:151] op_sel_hi:[0,1,1]
	v_min_f32_e32 v58, 0x41898193, v58
	v_min_f32_e32 v59, 0x41898193, v59
	v_exp_f32_e64 v68, -v58
	v_exp_f32_e64 v69, -v59
	v_pk_fma_f32 v[60:61], v[66:67], v[60:61], v[156:157] op_sel_hi:[0,1,1]
	v_pk_fma_f32 v[62:63], v[66:67], v[62:63], v[152:153] op_sel_hi:[0,1,1]
	v_pk_fma_f32 v[64:65], v[66:67], v[64:65], v[154:155] op_sel_hi:[0,1,1]
	v_pk_add_f32 v[68:69], v[68:69], 1.0 op_sel_hi:[1,0]
	v_med3_f32 v62, v62, s70, v167
	v_rcp_f32_e32 v68, v68
	v_rcp_f32_e32 v69, v69
	v_med3_f32 v63, v63, s70, v167
	v_min_f32_e32 v60, 0x41898193, v60
	v_min_f32_e32 v61, 0x41898193, v61
	v_pk_mul_f32 v[58:59], v[58:59], v[68:69]
	v_pk_fma_f32 v[50:51], v[66:67], v[50:51], v[86:87] op_sel_hi:[0,1,1]
	v_pk_mul_f32 v[58:59], v[58:59], v[62:63]
	v_med3_f32 v62, v64, s70, v167
	v_med3_f32 v63, v65, s70, v167
	v_exp_f32_e64 v64, -v60
	v_exp_f32_e64 v65, -v61
	v_min_f32_e32 v50, 0x41898193, v50
	v_min_f32_e32 v51, 0x41898193, v51
	v_pk_fma_f32 v[52:53], v[66:67], v[52:53], v[88:89] op_sel_hi:[0,1,1]
	v_pk_add_f32 v[64:65], v[64:65], 1.0 op_sel_hi:[1,0]
	v_pk_fma_f32 v[54:55], v[66:67], v[54:55], v[82:83] op_sel_hi:[0,1,1]
	v_rcp_f32_e32 v64, v64
	v_rcp_f32_e32 v65, v65
	v_pk_fma_f32 v[56:57], v[66:67], v[56:57], v[84:85] op_sel_hi:[0,1,1]
	v_med3_f32 v54, v54, s70, v167
	v_med3_f32 v55, v55, s70, v167
	v_pk_mul_f32 v[60:61], v[60:61], v[64:65]
	v_min_f32_e32 v52, 0x41898193, v52
	v_pk_mul_f32 v[60:61], v[60:61], v[62:63]
	v_exp_f32_e64 v62, -v50
	v_exp_f32_e64 v63, -v51
	v_min_f32_e32 v53, 0x41898193, v53
	v_pk_add_f32 v[62:63], v[62:63], 1.0 op_sel_hi:[1,0]
	s_nop 0
	v_rcp_f32_e32 v62, v62
	v_rcp_f32_e32 v63, v63
	s_nop 0
	v_pk_mul_f32 v[50:51], v[50:51], v[62:63]
	s_nop 0
	v_pk_mul_f32 v[50:51], v[50:51], v[54:55]
	v_med3_f32 v54, v56, s70, v167
	v_med3_f32 v55, v57, s70, v167
	v_exp_f32_e64 v56, -v52
	v_exp_f32_e64 v57, -v53
	s_nop 0
	v_pk_add_f32 v[56:57], v[56:57], 1.0 op_sel_hi:[1,0]
	s_nop 0
	v_rcp_f32_e32 v56, v56
	v_rcp_f32_e32 v57, v57
	s_nop 0
	v_pk_mul_f32 v[52:53], v[52:53], v[56:57]
	s_nop 0
	v_pk_mul_f32 v[52:53], v[52:53], v[54:55]
	v_mov_b32_e32 v55, v143
	v_cvt_pk_fp8_f32 v55, v50, v51
	v_mul_f32_e32 v50, 0x3d800000, v172
	v_pk_fma_f32 v[42:43], v[50:51], v[42:43], v[150:151] op_sel_hi:[0,1,1]
	v_min_f32_e32 v42, 0x41898193, v42
	v_min_f32_e32 v43, 0x41898193, v43
	v_cvt_pk_fp8_f32 v55, v52, v53 op_sel:[0,0,1]
	v_exp_f32_e64 v52, -v42
	v_exp_f32_e64 v53, -v43
	v_pk_fma_f32 v[44:45], v[50:51], v[44:45], v[156:157] op_sel_hi:[0,1,1]
	v_pk_fma_f32 v[46:47], v[50:51], v[46:47], v[152:153] op_sel_hi:[0,1,1]
	v_pk_fma_f32 v[48:49], v[50:51], v[48:49], v[154:155] op_sel_hi:[0,1,1]
	v_pk_add_f32 v[52:53], v[52:53], 1.0 op_sel_hi:[1,0]
	v_med3_f32 v46, v46, s70, v167
	v_rcp_f32_e32 v52, v52
	v_rcp_f32_e32 v53, v53
	v_med3_f32 v47, v47, s70, v167
	v_min_f32_e32 v44, 0x41898193, v44
	v_min_f32_e32 v45, 0x41898193, v45
	v_pk_mul_f32 v[42:43], v[42:43], v[52:53]
	v_pk_fma_f32 v[34:35], v[50:51], v[34:35], v[86:87] op_sel_hi:[0,1,1]
	v_pk_mul_f32 v[42:43], v[42:43], v[46:47]
	v_med3_f32 v46, v48, s70, v167
	v_med3_f32 v47, v49, s70, v167
	v_exp_f32_e64 v48, -v44
	v_exp_f32_e64 v49, -v45
	v_min_f32_e32 v34, 0x41898193, v34
	v_min_f32_e32 v35, 0x41898193, v35
	v_pk_fma_f32 v[36:37], v[50:51], v[36:37], v[88:89] op_sel_hi:[0,1,1]
	v_pk_add_f32 v[48:49], v[48:49], 1.0 op_sel_hi:[1,0]
	v_pk_fma_f32 v[38:39], v[50:51], v[38:39], v[82:83] op_sel_hi:[0,1,1]
	v_rcp_f32_e32 v48, v48
	v_rcp_f32_e32 v49, v49
	v_pk_fma_f32 v[40:41], v[50:51], v[40:41], v[84:85] op_sel_hi:[0,1,1]
	v_med3_f32 v38, v38, s70, v167
	v_med3_f32 v39, v39, s70, v167
	v_pk_mul_f32 v[44:45], v[44:45], v[48:49]
	v_min_f32_e32 v36, 0x41898193, v36
	v_pk_mul_f32 v[44:45], v[44:45], v[46:47]
	v_exp_f32_e64 v46, -v34
	v_exp_f32_e64 v47, -v35
	v_min_f32_e32 v37, 0x41898193, v37
	v_mov_b32_e32 v54, v143
	v_cvt_pk_fp8_f32 v54, v58, v59
	v_pk_add_f32 v[46:47], v[46:47], 1.0 op_sel_hi:[1,0]
	v_cvt_pk_fp8_f32 v54, v60, v61 op_sel:[0,0,1]
	v_rcp_f32_e32 v46, v46
	v_rcp_f32_e32 v47, v47
	ds_write_b64 v122, v[54:55]
	v_pk_mul_f32 v[34:35], v[34:35], v[46:47]
	s_nop 0
	v_pk_mul_f32 v[34:35], v[34:35], v[38:39]
	v_med3_f32 v38, v40, s70, v167
	v_med3_f32 v39, v41, s70, v167
	v_exp_f32_e64 v40, -v36
	v_exp_f32_e64 v41, -v37
	s_nop 0
	v_pk_add_f32 v[40:41], v[40:41], 1.0 op_sel_hi:[1,0]
	s_nop 0
	v_rcp_f32_e32 v40, v40
	v_rcp_f32_e32 v41, v41
	s_nop 0
	v_pk_mul_f32 v[36:37], v[36:37], v[40:41]
	s_nop 0
	v_pk_mul_f32 v[36:37], v[36:37], v[38:39]
	v_mov_b32_e32 v38, v143
	v_mov_b32_e32 v39, v143
	v_cvt_pk_fp8_f32 v38, v42, v43
	v_cvt_pk_fp8_f32 v39, v34, v35
	v_cvt_pk_fp8_f32 v38, v44, v45 op_sel:[0,0,1]
	v_cvt_pk_fp8_f32 v39, v36, v37 op_sel:[0,0,1]
	ds_write_b64 v122, v[38:39] offset:768
	v_add_u32_e32 v38, 0x80, v106
	ds_read_b128 v[34:37], v108
	v_ashrrev_i32_e32 v39, 31, v38
	v_lshlrev_b64 v[38:39], 10, v[38:39]
	v_lshl_add_u64 v[38:39], s[16:17], 0, v[38:39]
	v_lshl_add_u64 v[38:39], v[38:39], 0, s[8:9]
	v_lshl_add_u64 v[38:39], v[38:39], 0, v[142:143]
	s_waitcnt lgkmcnt(0)
	global_store_dwordx4 v[38:39], v[34:37], off
	s_nop 1
	v_mul_f32_e32 v34, 0x3d800000, v171
	v_pk_fma_f32 v[26:27], v[34:35], v[26:27], v[150:151] op_sel_hi:[0,1,1]
	v_min_f32_e32 v26, 0x41898193, v26
	v_min_f32_e32 v27, 0x41898193, v27
	v_exp_f32_e64 v36, -v26
	v_exp_f32_e64 v37, -v27
	v_pk_fma_f32 v[28:29], v[34:35], v[28:29], v[156:157] op_sel_hi:[0,1,1]
	v_pk_fma_f32 v[30:31], v[34:35], v[30:31], v[152:153] op_sel_hi:[0,1,1]
	v_pk_fma_f32 v[32:33], v[34:35], v[32:33], v[154:155] op_sel_hi:[0,1,1]
	v_pk_add_f32 v[36:37], v[36:37], 1.0 op_sel_hi:[1,0]
	v_med3_f32 v30, v30, s70, v167
	v_rcp_f32_e32 v36, v36
	v_rcp_f32_e32 v37, v37
	v_med3_f32 v31, v31, s70, v167
	v_min_f32_e32 v28, 0x41898193, v28
	v_min_f32_e32 v29, 0x41898193, v29
	v_pk_mul_f32 v[26:27], v[26:27], v[36:37]
	v_pk_fma_f32 v[18:19], v[34:35], v[18:19], v[86:87] op_sel_hi:[0,1,1]
	v_pk_mul_f32 v[26:27], v[26:27], v[30:31]
	v_med3_f32 v30, v32, s70, v167
	v_med3_f32 v31, v33, s70, v167
	v_exp_f32_e64 v32, -v28
	v_exp_f32_e64 v33, -v29
	v_min_f32_e32 v18, 0x41898193, v18
	v_min_f32_e32 v19, 0x41898193, v19
	v_pk_fma_f32 v[20:21], v[34:35], v[20:21], v[88:89] op_sel_hi:[0,1,1]
	v_pk_add_f32 v[32:33], v[32:33], 1.0 op_sel_hi:[1,0]
	v_pk_fma_f32 v[22:23], v[34:35], v[22:23], v[82:83] op_sel_hi:[0,1,1]
	v_rcp_f32_e32 v32, v32
	v_rcp_f32_e32 v33, v33
	v_pk_fma_f32 v[24:25], v[34:35], v[24:25], v[84:85] op_sel_hi:[0,1,1]
	v_med3_f32 v22, v22, s70, v167
	v_med3_f32 v23, v23, s70, v167
	v_pk_mul_f32 v[28:29], v[28:29], v[32:33]
	v_min_f32_e32 v20, 0x41898193, v20
	v_pk_mul_f32 v[28:29], v[28:29], v[30:31]
	v_exp_f32_e64 v30, -v18
	v_exp_f32_e64 v31, -v19
	v_min_f32_e32 v21, 0x41898193, v21
	v_pk_add_f32 v[30:31], v[30:31], 1.0 op_sel_hi:[1,0]
	s_nop 0
	v_rcp_f32_e32 v30, v30
	v_rcp_f32_e32 v31, v31
	s_nop 0
	v_pk_mul_f32 v[18:19], v[18:19], v[30:31]
	s_nop 0
	v_pk_mul_f32 v[18:19], v[18:19], v[22:23]
	v_med3_f32 v22, v24, s70, v167
	v_med3_f32 v23, v25, s70, v167
	v_exp_f32_e64 v24, -v20
	v_exp_f32_e64 v25, -v21
	s_nop 0
	v_pk_add_f32 v[24:25], v[24:25], 1.0 op_sel_hi:[1,0]
	s_nop 0
	v_rcp_f32_e32 v24, v24
	v_rcp_f32_e32 v25, v25
	s_nop 0
	v_pk_mul_f32 v[20:21], v[20:21], v[24:25]
	s_nop 0
	v_pk_mul_f32 v[20:21], v[20:21], v[22:23]
	v_mov_b32_e32 v23, v143
	v_cvt_pk_fp8_f32 v23, v18, v19
	v_mul_f32_e32 v18, 0x3d800000, v168
	v_pk_fma_f32 v[10:11], v[18:19], v[10:11], v[150:151] op_sel_hi:[0,1,1]
	v_min_f32_e32 v10, 0x41898193, v10
	v_min_f32_e32 v11, 0x41898193, v11
	v_cvt_pk_fp8_f32 v23, v20, v21 op_sel:[0,0,1]
	v_exp_f32_e64 v20, -v10
	v_exp_f32_e64 v21, -v11
	v_pk_fma_f32 v[12:13], v[18:19], v[12:13], v[156:157] op_sel_hi:[0,1,1]
	v_pk_fma_f32 v[14:15], v[18:19], v[14:15], v[152:153] op_sel_hi:[0,1,1]
	v_pk_fma_f32 v[16:17], v[18:19], v[16:17], v[154:155] op_sel_hi:[0,1,1]
	v_pk_add_f32 v[20:21], v[20:21], 1.0 op_sel_hi:[1,0]
	v_med3_f32 v14, v14, s70, v167
	v_rcp_f32_e32 v20, v20
	v_rcp_f32_e32 v21, v21
	v_med3_f32 v15, v15, s70, v167
	v_min_f32_e32 v12, 0x41898193, v12
	v_min_f32_e32 v13, 0x41898193, v13
	v_pk_mul_f32 v[10:11], v[10:11], v[20:21]
	v_pk_fma_f32 v[2:3], v[18:19], v[2:3], v[86:87] op_sel_hi:[0,1,1]
	v_pk_mul_f32 v[10:11], v[10:11], v[14:15]
	v_med3_f32 v14, v16, s70, v167
	v_med3_f32 v15, v17, s70, v167
	v_exp_f32_e64 v16, -v12
	v_exp_f32_e64 v17, -v13
	v_min_f32_e32 v2, 0x41898193, v2
	v_min_f32_e32 v3, 0x41898193, v3
	v_pk_fma_f32 v[4:5], v[18:19], v[4:5], v[88:89] op_sel_hi:[0,1,1]
	v_pk_add_f32 v[16:17], v[16:17], 1.0 op_sel_hi:[1,0]
	v_pk_fma_f32 v[6:7], v[18:19], v[6:7], v[82:83] op_sel_hi:[0,1,1]
	v_rcp_f32_e32 v16, v16
	v_rcp_f32_e32 v17, v17
	v_pk_fma_f32 v[8:9], v[18:19], v[8:9], v[84:85] op_sel_hi:[0,1,1]
	v_med3_f32 v6, v6, s70, v167
	v_med3_f32 v7, v7, s70, v167
	v_pk_mul_f32 v[12:13], v[12:13], v[16:17]
	v_min_f32_e32 v4, 0x41898193, v4
	v_pk_mul_f32 v[12:13], v[12:13], v[14:15]
	v_exp_f32_e64 v14, -v2
	v_exp_f32_e64 v15, -v3
	v_min_f32_e32 v5, 0x41898193, v5
	v_mov_b32_e32 v22, v143
	v_cvt_pk_fp8_f32 v22, v26, v27
	v_pk_add_f32 v[14:15], v[14:15], 1.0 op_sel_hi:[1,0]
	v_cvt_pk_fp8_f32 v22, v28, v29 op_sel:[0,0,1]
	v_rcp_f32_e32 v14, v14
	v_rcp_f32_e32 v15, v15
	ds_write_b64 v122, v[22:23]
	v_pk_mul_f32 v[2:3], v[2:3], v[14:15]
	s_nop 0
	v_pk_mul_f32 v[2:3], v[2:3], v[6:7]
	v_med3_f32 v6, v8, s70, v167
	v_med3_f32 v7, v9, s70, v167
	v_exp_f32_e64 v8, -v4
	v_exp_f32_e64 v9, -v5
	s_nop 0
	v_pk_add_f32 v[8:9], v[8:9], 1.0 op_sel_hi:[1,0]
	s_nop 0
	v_rcp_f32_e32 v8, v8
	v_rcp_f32_e32 v9, v9
	s_nop 0
	v_pk_mul_f32 v[4:5], v[4:5], v[8:9]
	s_nop 0
	v_pk_mul_f32 v[4:5], v[4:5], v[6:7]
	v_mov_b32_e32 v6, v143
	v_mov_b32_e32 v7, v143
	v_cvt_pk_fp8_f32 v6, v10, v11
	v_cvt_pk_fp8_f32 v7, v2, v3
	v_cvt_pk_fp8_f32 v6, v12, v13 op_sel:[0,0,1]
	v_cvt_pk_fp8_f32 v7, v4, v5 op_sel:[0,0,1]
	ds_write_b64 v122, v[6:7] offset:768
	v_add_u32_e32 v6, 0xa0, v106
	ds_read_b128 v[2:5], v108
	v_ashrrev_i32_e32 v7, 31, v6
	v_lshlrev_b64 v[6:7], 10, v[6:7]
	v_lshl_add_u64 v[6:7], s[16:17], 0, v[6:7]
	v_lshl_add_u64 v[6:7], v[6:7], 0, s[8:9]
	v_lshl_add_u64 v[6:7], v[6:7], 0, v[142:143]
	s_mov_b64 s[8:9], -1
	s_waitcnt lgkmcnt(0)
	global_store_dwordx4 v[6:7], v[2:5], off
	s_cbranch_vccnz .LBB0_1537
	s_lshl_b64 s[6:7], s[74:75], 12
	s_add_u32 s9, s33, s6
	s_addc_u32 s69, s54, s7
	s_lshl_b32 s6, s68, 7
	s_ashr_i32 s7, s6, 31
	v_mov_b32_e32 v2, v0
	s_lshl_b64 s[6:7], s[6:7], 1
	s_add_u32 s6, s9, s6
	v_readfirstlane_b32 s8, v2
	s_addc_u32 s7, s69, s7
	s_and_b32 s9, s8, 0xc0
	s_add_u32 s6, s6, s9
	s_addc_u32 s7, s7, 0
	v_and_b32_e32 v3, 48, v2
	global_load_dwordx4 v[86:89], v3, s[6:7]
	global_load_dwordx4 v[82:85], v3, s[6:7] offset:2048
	s_ashr_i32 s7, s8, 2
	s_lshl_b32 s6, s72, 8
	s_andn2_b32 s7, s7, 63
	s_add_i32 s7, s7, s6
	v_and_or_b32 v2, v2, 15, s7
	v_ashrrev_i32_e32 v3, 31, v2
	v_lshl_add_u64 v[4:5], v[2:3], 2, s[12:13]
	v_add_u32_e32 v6, 0x80, v2
	v_add_u32_e32 v8, 0x90, v2
	v_add_u32_e32 v10, 0xa0, v2
	v_add_u32_e32 v2, 0xb0, v2
	v_ashrrev_i32_e32 v7, 31, v6
	v_ashrrev_i32_e32 v9, 31, v8
	v_ashrrev_i32_e32 v11, 31, v10
	v_ashrrev_i32_e32 v3, 31, v2
	v_lshl_add_u64 v[6:7], v[6:7], 2, s[12:13]
	v_lshl_add_u64 v[8:9], v[8:9], 2, s[12:13]
	v_lshl_add_u64 v[10:11], v[10:11], 2, s[12:13]
	v_lshl_add_u64 v[2:3], v[2:3], 2, s[12:13]
	global_load_dword v177, v[4:5], off
	global_load_dword v176, v[4:5], off offset:64
	global_load_dword v175, v[4:5], off offset:128
	global_load_dword v174, v[4:5], off offset:192
	global_load_dword v173, v[6:7], off
	global_load_dword v172, v[8:9], off
	global_load_dword v171, v[10:11], off
	global_load_dword v168, v[2:3], off
	s_andn2_b64 vcc, exec, s[14:15]
	s_cbranch_vccnz .LBB0_1536
	s_barrier
	s_branch .LBB0_1536

.LBB0_1627:
	v_lshlrev_b32_e32 v158, 16, v6
	v_and_b32_e32 v159, 0xffff0000, v6
	v_lshlrev_b32_e32 v154, 16, v8
	v_and_b32_e32 v155, 0xffff0000, v8
	v_lshlrev_b32_e32 v156, 16, v7
	v_and_b32_e32 v157, 0xffff0000, v7
	v_lshlrev_b32_e32 v152, 16, v9
	v_and_b32_e32 v153, 0xffff0000, v9
	s_waitcnt vmcnt(10)
	v_lshlrev_b32_e32 v6, 16, v4
	v_and_b32_e32 v7, 0xffff0000, v4
	v_mul_f32_e32 v4, 0x41000000, v146
	v_pk_fma_f32 v[134:135], v[134:135], s[36:37], v[158:159] op_sel_hi:[1,0,1]
	v_pk_fma_f32 v[130:131], v[130:131], s[36:37], v[154:155] op_sel_hi:[1,0,1]
	v_pk_fma_f32 v[136:137], v[136:137], s[36:37], v[156:157] op_sel_hi:[1,0,1]
	v_pk_mul_f32 v[134:135], v[4:5], v[134:135] op_sel_hi:[0,1]
	v_pk_fma_f32 v[132:133], v[132:133], s[36:37], v[152:153] op_sel_hi:[1,0,1]
	v_pk_mul_f32 v[130:131], v[4:5], v[130:131] op_sel_hi:[0,1]
	v_lshlrev_b32_e32 v150, 16, v2
	v_and_b32_e32 v151, 0xffff0000, v2
	v_lshlrev_b32_e32 v8, 16, v3
	v_and_b32_e32 v9, 0xffff0000, v3
	v_lshlrev_b32_e32 v2, 16, v5
	v_and_b32_e32 v3, 0xffff0000, v5
	v_pk_mul_f32 v[136:137], v[4:5], v[136:137] op_sel_hi:[0,1]
	v_pk_mul_f32 v[132:133], v[4:5], v[132:133] op_sel_hi:[0,1]
	v_med3_f32 v5, v134, s70, v164
	v_med3_f32 v134, v130, s70, v164
	v_med3_f32 v135, v135, s70, v164
	v_mov_b32_e32 v130, 0
	v_cvt_pk_fp8_f32 v130, v5, v135
	v_med3_f32 v136, v136, s70, v164
	v_med3_f32 v5, v137, s70, v164
	v_pk_fma_f32 v[126:127], v[126:127], s[36:37], v[150:151] op_sel_hi:[1,0,1]
	v_pk_fma_f32 v[128:129], v[128:129], s[36:37], v[8:9] op_sel_hi:[1,0,1]
	v_pk_fma_f32 v[122:123], v[122:123], s[36:37], v[6:7] op_sel_hi:[1,0,1]
	v_pk_fma_f32 v[124:125], v[124:125], s[36:37], v[2:3] op_sel_hi:[1,0,1]
	v_cvt_pk_fp8_f32 v130, v136, v5 op_sel:[0,0,1]
	v_pk_mul_f32 v[128:129], v[4:5], v[128:129] op_sel_hi:[0,1]
	v_pk_mul_f32 v[126:127], v[4:5], v[126:127] op_sel_hi:[0,1]
	v_pk_mul_f32 v[124:125], v[4:5], v[124:125] op_sel_hi:[0,1]
	v_pk_mul_f32 v[4:5], v[4:5], v[122:123] op_sel_hi:[0,1]
	v_med3_f32 v146, v131, s70, v164
	v_mov_b32_e32 v131, 0
	v_med3_f32 v122, v126, s70, v164
	v_med3_f32 v123, v4, s70, v164
	v_med3_f32 v126, v127, s70, v164
	v_med3_f32 v127, v5, s70, v164
	v_mov_b32_e32 v4, 0
	v_mov_b32_e32 v5, 0
	v_cvt_pk_fp8_f32 v131, v134, v146
	v_cvt_pk_fp8_f32 v4, v122, v126
	v_cvt_pk_fp8_f32 v5, v123, v127
	v_mov_b32_e32 v171, v0
	v_med3_f32 v132, v132, s70, v164
	v_readfirstlane_b32 s39, v171
	s_lshr_b32 s6, s39, 6
	v_med3_f32 v133, v133, s70, v164
	v_med3_f32 v128, v128, s70, v164
	v_med3_f32 v124, v124, s70, v164
	v_med3_f32 v122, v129, s70, v164
	v_med3_f32 v123, v125, s70, v164
	s_mulk_i32 s6, 0xb00
	v_cvt_pk_fp8_f32 v131, v132, v133 op_sel:[0,0,1]
	v_cvt_pk_fp8_f32 v4, v128, v122 op_sel:[0,0,1]
	v_cvt_pk_fp8_f32 v5, v124, v123 op_sel:[0,0,1]
	s_add_i32 s6, s6, 0
	v_and_b32_e32 v172, 15, v171
	v_lshrrev_b32_e32 v123, 1, v171
	s_add_i32 s41, s6, 0x20000
	v_mul_u32_u24_e32 v122, 0x50, v172
	v_and_b32_e32 v123, 24, v123
	v_add3_u32 v122, s41, v122, v123
	s_and_b32 s7, s39, 0xc0
	ds_write2_b64 v122, v[130:131], v[4:5] offset1:4
	v_bfe_u32 v4, v171, 2, 4
	s_ashr_i32 s39, s39, 2
	v_mul_u32_u24_e32 v5, 0x50, v4
	v_lshlrev_b32_e32 v123, 4, v171
	s_andn2_b32 s39, s39, 63
	v_lshl_or_b32 v4, s48, 8, v4
	v_and_b32_e32 v146, 48, v123
	v_add_u32_e32 v4, s39, v4
	v_mul_f32_e32 v130, 0x41000000, v170
	v_pk_fma_f32 v[118:119], v[118:119], s[36:37], v[158:159] op_sel_hi:[1,0,1]
	v_pk_fma_f32 v[114:115], v[114:115], s[36:37], v[154:155] op_sel_hi:[1,0,1]
	v_add3_u32 v123, s41, v5, v146
	v_ashrrev_i32_e32 v5, 31, v4
	v_pk_mul_f32 v[118:119], v[130:131], v[118:119] op_sel_hi:[0,1]
	v_pk_mul_f32 v[114:115], v[130:131], v[114:115] op_sel_hi:[0,1]
	v_lshlrev_b64 v[128:129], 10, v[4:5]
	v_med3_f32 v5, v118, s70, v164
	v_med3_f32 v118, v114, s70, v164
	v_med3_f32 v119, v119, s70, v164
	v_mov_b32_e32 v114, v147
	v_cvt_pk_fp8_f32 v114, v5, v119
	v_pk_fma_f32 v[120:121], v[120:121], s[36:37], v[156:157] op_sel_hi:[1,0,1]
	v_pk_fma_f32 v[116:117], v[116:117], s[36:37], v[152:153] op_sel_hi:[1,0,1]
	v_pk_mul_f32 v[120:121], v[130:131], v[120:121] op_sel_hi:[0,1]
	v_pk_mul_f32 v[116:117], v[130:131], v[116:117] op_sel_hi:[0,1]
	v_med3_f32 v131, v115, s70, v164
	v_pk_fma_f32 v[110:111], v[110:111], s[36:37], v[150:151] op_sel_hi:[1,0,1]
	v_pk_fma_f32 v[106:107], v[106:107], s[36:37], v[6:7] op_sel_hi:[1,0,1]
	v_med3_f32 v120, v120, s70, v164
	v_med3_f32 v5, v121, s70, v164
	v_pk_mul_f32 v[110:111], v[130:131], v[110:111] op_sel_hi:[0,1]
	v_pk_mul_f32 v[106:107], v[130:131], v[106:107] op_sel_hi:[0,1]
	v_cvt_pk_fp8_f32 v114, v120, v5 op_sel:[0,0,1]
	v_med3_f32 v5, v110, s70, v164
	v_med3_f32 v110, v106, s70, v164
	v_med3_f32 v111, v111, s70, v164
	v_mov_b32_e32 v106, v147
	v_cvt_pk_fp8_f32 v106, v5, v111
	v_pk_fma_f32 v[112:113], v[112:113], s[36:37], v[8:9] op_sel_hi:[1,0,1]
	v_mov_b32_e32 v115, v147
	v_pk_mul_f32 v[112:113], v[130:131], v[112:113] op_sel_hi:[0,1]
	v_med3_f32 v112, v112, s70, v164
	v_med3_f32 v5, v113, s70, v164
	v_cvt_pk_fp8_f32 v106, v112, v5 op_sel:[0,0,1]
	v_mul_f32_e32 v112, 0x41000000, v169
	v_pk_fma_f32 v[102:103], v[102:103], s[36:37], v[158:159] op_sel_hi:[1,0,1]
	v_pk_fma_f32 v[98:99], v[98:99], s[36:37], v[154:155] op_sel_hi:[1,0,1]
	v_cvt_pk_fp8_f32 v115, v118, v131
	v_pk_mul_f32 v[102:103], v[112:113], v[102:103] op_sel_hi:[0,1]
	v_pk_mul_f32 v[98:99], v[112:113], v[98:99] op_sel_hi:[0,1]
	v_med3_f32 v5, v102, s70, v164
	v_med3_f32 v102, v98, s70, v164
	v_med3_f32 v103, v103, s70, v164
	v_mov_b32_e32 v98, v147
	v_cvt_pk_fp8_f32 v98, v5, v103
	v_med3_f32 v116, v116, s70, v164
	v_med3_f32 v117, v117, s70, v164
	v_pk_fma_f32 v[104:105], v[104:105], s[36:37], v[156:157] op_sel_hi:[1,0,1]
	v_pk_fma_f32 v[100:101], v[100:101], s[36:37], v[152:153] op_sel_hi:[1,0,1]
	v_cvt_pk_fp8_f32 v115, v116, v117 op_sel:[0,0,1]
	v_med3_f32 v116, v107, s70, v164
	v_mov_b32_e32 v107, v147
	v_pk_mul_f32 v[104:105], v[112:113], v[104:105] op_sel_hi:[0,1]
	v_pk_mul_f32 v[100:101], v[112:113], v[100:101] op_sel_hi:[0,1]
	v_med3_f32 v113, v99, s70, v164
	v_pk_fma_f32 v[94:95], v[94:95], s[36:37], v[150:151] op_sel_hi:[1,0,1]
	v_pk_fma_f32 v[90:91], v[90:91], s[36:37], v[6:7] op_sel_hi:[1,0,1]
	v_cvt_pk_fp8_f32 v107, v110, v116
	v_med3_f32 v104, v104, s70, v164
	v_med3_f32 v5, v105, s70, v164
	v_pk_mul_f32 v[94:95], v[112:113], v[94:95] op_sel_hi:[0,1]
	v_pk_mul_f32 v[90:91], v[112:113], v[90:91] op_sel_hi:[0,1]
	v_pk_fma_f32 v[108:109], v[108:109], s[36:37], v[2:3] op_sel_hi:[1,0,1]
	v_mov_b32_e32 v99, v147
	v_cvt_pk_fp8_f32 v98, v104, v5 op_sel:[0,0,1]
	v_med3_f32 v5, v94, s70, v164
	v_med3_f32 v94, v90, s70, v164
	v_med3_f32 v95, v95, s70, v164
	v_mov_b32_e32 v90, v147
	s_lshl_b32 s6, s50, 8
	ds_read_b128 v[124:127], v123
	v_pk_mul_f32 v[108:109], v[130:131], v[108:109] op_sel_hi:[0,1]
	v_cvt_pk_fp8_f32 v99, v102, v113
	v_cvt_pk_fp8_f32 v90, v5, v95
	s_or_b32 s6, s7, s6
	v_med3_f32 v108, v108, s70, v164
	v_med3_f32 v109, v109, s70, v164
	v_pk_fma_f32 v[96:97], v[96:97], s[36:37], v[8:9] op_sel_hi:[1,0,1]
	s_ashr_i32 s7, s6, 31
	v_lshl_add_u64 v[128:129], s[16:17], 0, v[128:129]
	v_cvt_pk_fp8_f32 v107, v108, v109 op_sel:[0,0,1]
	v_pk_mul_f32 v[96:97], v[112:113], v[96:97] op_sel_hi:[0,1]
	v_lshl_add_u64 v[128:129], v[128:129], 0, s[6:7]
	v_med3_f32 v100, v100, s70, v164
	v_med3_f32 v101, v101, s70, v164
	v_med3_f32 v96, v96, s70, v164
	v_med3_f32 v5, v97, s70, v164
	v_lshl_add_u64 v[108:109], v[128:129], 0, v[146:147]
	v_cvt_pk_fp8_f32 v99, v100, v101 op_sel:[0,0,1]
	v_med3_f32 v100, v91, s70, v164
	v_mov_b32_e32 v91, v147
	v_cvt_pk_fp8_f32 v90, v96, v5 op_sel:[0,0,1]
	v_mul_f32_e32 v96, 0x41000000, v168
	v_pk_fma_f32 v[78:79], v[78:79], s[36:37], v[158:159] op_sel_hi:[1,0,1]
	v_pk_fma_f32 v[74:75], v[74:75], s[36:37], v[154:155] op_sel_hi:[1,0,1]
	s_waitcnt lgkmcnt(0)
	global_store_dwordx4 v[108:109], v[124:127], off
	v_cvt_pk_fp8_f32 v91, v94, v100
	v_pk_fma_f32 v[80:81], v[80:81], s[36:37], v[156:157] op_sel_hi:[1,0,1]
	v_pk_mul_f32 v[78:79], v[96:97], v[78:79] op_sel_hi:[0,1]
	v_pk_fma_f32 v[76:77], v[76:77], s[36:37], v[152:153] op_sel_hi:[1,0,1]
	v_pk_mul_f32 v[74:75], v[96:97], v[74:75] op_sel_hi:[0,1]
	ds_write2_b64 v122, v[114:115], v[106:107] offset1:4
	v_or_b32_e32 v110, 16, v4
	v_pk_fma_f32 v[92:93], v[92:93], s[36:37], v[2:3] op_sel_hi:[1,0,1]
	v_pk_mul_f32 v[80:81], v[96:97], v[80:81] op_sel_hi:[0,1]
	v_pk_mul_f32 v[76:77], v[96:97], v[76:77] op_sel_hi:[0,1]
	v_med3_f32 v5, v78, s70, v164
	v_med3_f32 v78, v74, s70, v164
	v_med3_f32 v79, v79, s70, v164
	v_med3_f32 v97, v75, s70, v164
	v_mov_b32_e32 v74, v147
	v_mov_b32_e32 v75, v147
	ds_read_b128 v[106:109], v123
	v_ashrrev_i32_e32 v111, 31, v110
	v_pk_mul_f32 v[92:93], v[112:113], v[92:93] op_sel_hi:[0,1]
	v_cvt_pk_fp8_f32 v74, v5, v79
	v_cvt_pk_fp8_f32 v75, v78, v97
	v_lshlrev_b64 v[110:111], 10, v[110:111]
	v_med3_f32 v92, v92, s70, v164
	v_med3_f32 v93, v93, s70, v164
	v_lshl_add_u64 v[110:111], s[16:17], 0, v[110:111]
	v_cvt_pk_fp8_f32 v91, v92, v93 op_sel:[0,0,1]
	v_pk_fma_f32 v[62:63], v[62:63], s[36:37], v[150:151] op_sel_hi:[1,0,1]
	v_pk_fma_f32 v[58:59], v[58:59], s[36:37], v[6:7] op_sel_hi:[1,0,1]
	v_lshl_add_u64 v[110:111], v[110:111], 0, s[6:7]
	v_med3_f32 v80, v80, s70, v164
	v_med3_f32 v76, v76, s70, v164
	v_med3_f32 v5, v81, s70, v164
	v_med3_f32 v77, v77, s70, v164
	v_pk_mul_f32 v[62:63], v[96:97], v[62:63] op_sel_hi:[0,1]
	v_pk_mul_f32 v[58:59], v[96:97], v[58:59] op_sel_hi:[0,1]
	v_lshl_add_u64 v[92:93], v[110:111], 0, v[146:147]
	v_cvt_pk_fp8_f32 v74, v80, v5 op_sel:[0,0,1]
	v_cvt_pk_fp8_f32 v75, v76, v77 op_sel:[0,0,1]
	v_med3_f32 v5, v62, s70, v164
	v_med3_f32 v62, v58, s70, v164
	v_med3_f32 v63, v63, s70, v164
	v_med3_f32 v76, v59, s70, v164
	v_mov_b32_e32 v58, v147
	v_mov_b32_e32 v59, v147
	s_waitcnt lgkmcnt(0)
	global_store_dwordx4 v[92:93], v[106:109], off
	s_cmp_lg_u64 s[10:11], 0
	s_cbranch_scc0 .Lepibar_dn0
	s_barrier
.Lepibar_dn0:
	v_cvt_pk_fp8_f32 v58, v5, v63
	v_cvt_pk_fp8_f32 v59, v62, v76
	ds_write2_b64 v122, v[98:99], v[90:91] offset1:4
	v_or_b32_e32 v94, 32, v4
	v_pk_fma_f32 v[64:65], v[64:65], s[36:37], v[8:9] op_sel_hi:[1,0,1]
	v_pk_fma_f32 v[60:61], v[60:61], s[36:37], v[2:3] op_sel_hi:[1,0,1]
	ds_read_b128 v[90:93], v123
	v_ashrrev_i32_e32 v95, 31, v94
	v_pk_mul_f32 v[64:65], v[96:97], v[64:65] op_sel_hi:[0,1]
	v_pk_mul_f32 v[60:61], v[96:97], v[60:61] op_sel_hi:[0,1]
	v_lshlrev_b64 v[94:95], 10, v[94:95]
	v_med3_f32 v64, v64, s70, v164
	v_med3_f32 v60, v60, s70, v164
	v_med3_f32 v5, v65, s70, v164
	v_med3_f32 v61, v61, s70, v164
	v_lshl_add_u64 v[94:95], s[16:17], 0, v[94:95]
	v_cvt_pk_fp8_f32 v58, v64, v5 op_sel:[0,0,1]
	v_cvt_pk_fp8_f32 v59, v60, v61 op_sel:[0,0,1]
	v_lshl_add_u64 v[94:95], v[94:95], 0, s[6:7]
	v_lshl_add_u64 v[60:61], v[94:95], 0, v[146:147]
	s_waitcnt lgkmcnt(0)
	global_store_dwordx4 v[60:61], v[90:93], off
	ds_write2_b64 v122, v[74:75], v[58:59] offset1:4
	v_mul_f32_e32 v64, 0x41000000, v167
	v_pk_fma_f32 v[74:75], v[86:87], s[36:37], v[158:159] op_sel_hi:[1,0,1]
	v_pk_fma_f32 v[78:79], v[82:83], s[36:37], v[154:155] op_sel_hi:[1,0,1]
	v_pk_mul_f32 v[74:75], v[64:65], v[74:75] op_sel_hi:[0,1]
	v_pk_fma_f32 v[76:77], v[88:89], s[36:37], v[156:157] op_sel_hi:[1,0,1]
	v_pk_fma_f32 v[80:81], v[84:85], s[36:37], v[152:153] op_sel_hi:[1,0,1]
	v_pk_mul_f32 v[78:79], v[64:65], v[78:79] op_sel_hi:[0,1]
	v_med3_f32 v5, v74, s70, v164
	v_med3_f32 v75, v75, s70, v164
	v_mov_b32_e32 v74, v147
	v_pk_mul_f32 v[76:77], v[64:65], v[76:77] op_sel_hi:[0,1]
	v_pk_mul_f32 v[80:81], v[64:65], v[80:81] op_sel_hi:[0,1]
	v_med3_f32 v65, v78, s70, v164
	v_med3_f32 v78, v79, s70, v164
	v_cvt_pk_fp8_f32 v74, v5, v75
	v_mov_b32_e32 v75, v147
	v_cvt_pk_fp8_f32 v75, v65, v78
	v_med3_f32 v79, v80, s70, v164
	v_med3_f32 v65, v81, s70, v164
	v_pk_fma_f32 v[70:71], v[70:71], s[36:37], v[150:151] op_sel_hi:[1,0,1]
	v_pk_fma_f32 v[72:73], v[72:73], s[36:37], v[8:9] op_sel_hi:[1,0,1]
	v_pk_fma_f32 v[66:67], v[66:67], s[36:37], v[6:7] op_sel_hi:[1,0,1]
	v_pk_fma_f32 v[68:69], v[68:69], s[36:37], v[2:3] op_sel_hi:[1,0,1]
	v_med3_f32 v76, v76, s70, v164
	v_med3_f32 v5, v77, s70, v164
	v_cvt_pk_fp8_f32 v75, v79, v65 op_sel:[0,0,1]
	v_pk_mul_f32 v[72:73], v[64:65], v[72:73] op_sel_hi:[0,1]
	v_pk_mul_f32 v[70:71], v[64:65], v[70:71] op_sel_hi:[0,1]
	v_pk_mul_f32 v[68:69], v[64:65], v[68:69] op_sel_hi:[0,1]
	v_pk_mul_f32 v[64:65], v[64:65], v[66:67] op_sel_hi:[0,1]
	v_cvt_pk_fp8_f32 v74, v76, v5 op_sel:[0,0,1]
	v_med3_f32 v5, v70, s70, v164
	v_med3_f32 v66, v64, s70, v164
	v_med3_f32 v67, v71, s70, v164
	v_med3_f32 v70, v65, s70, v164
	v_mov_b32_e32 v64, v147
	v_mov_b32_e32 v65, v147
	v_cvt_pk_fp8_f32 v64, v5, v67
	v_cvt_pk_fp8_f32 v65, v66, v70
	v_or_b32_e32 v62, 48, v4
	ds_read_b128 v[58:61], v123
	v_ashrrev_i32_e32 v63, 31, v62
	v_lshlrev_b64 v[62:63], 10, v[62:63]
	v_med3_f32 v71, v72, s70, v164
	v_med3_f32 v68, v68, s70, v164
	v_med3_f32 v5, v73, s70, v164
	v_med3_f32 v66, v69, s70, v164
	v_lshl_add_u64 v[62:63], s[16:17], 0, v[62:63]
	v_cvt_pk_fp8_f32 v64, v71, v5 op_sel:[0,0,1]
	v_cvt_pk_fp8_f32 v65, v68, v66 op_sel:[0,0,1]
	v_lshl_add_u64 v[62:63], v[62:63], 0, s[6:7]
	v_lshl_add_u64 v[62:63], v[62:63], 0, v[146:147]
	s_waitcnt lgkmcnt(0)
	global_store_dwordx4 v[62:63], v[58:61], off
	ds_write2_b64 v122, v[74:75], v[64:65] offset1:4
	v_mul_f32_e32 v64, 0x41000000, v166
	v_pk_fma_f32 v[54:55], v[54:55], s[36:37], v[158:159] op_sel_hi:[1,0,1]
	v_pk_fma_f32 v[50:51], v[50:51], s[36:37], v[154:155] op_sel_hi:[1,0,1]
	v_pk_mul_f32 v[54:55], v[64:65], v[54:55] op_sel_hi:[0,1]
	v_pk_mul_f32 v[50:51], v[64:65], v[50:51] op_sel_hi:[0,1]
	v_med3_f32 v5, v54, s70, v164
	v_med3_f32 v54, v50, s70, v164
	v_med3_f32 v55, v55, s70, v164
	v_mov_b32_e32 v50, v147
	v_cvt_pk_fp8_f32 v50, v5, v55
	v_pk_fma_f32 v[56:57], v[56:57], s[36:37], v[156:157] op_sel_hi:[1,0,1]
	v_pk_fma_f32 v[52:53], v[52:53], s[36:37], v[152:153] op_sel_hi:[1,0,1]
	v_pk_mul_f32 v[56:57], v[64:65], v[56:57] op_sel_hi:[0,1]
	v_pk_mul_f32 v[52:53], v[64:65], v[52:53] op_sel_hi:[0,1]
	v_med3_f32 v65, v51, s70, v164
	v_pk_fma_f32 v[46:47], v[46:47], s[36:37], v[150:151] op_sel_hi:[1,0,1]
	v_pk_fma_f32 v[42:43], v[42:43], s[36:37], v[6:7] op_sel_hi:[1,0,1]
	v_med3_f32 v56, v56, s70, v164
	v_med3_f32 v5, v57, s70, v164
	v_pk_mul_f32 v[46:47], v[64:65], v[46:47] op_sel_hi:[0,1]
	v_pk_mul_f32 v[42:43], v[64:65], v[42:43] op_sel_hi:[0,1]
	v_cvt_pk_fp8_f32 v50, v56, v5 op_sel:[0,0,1]
	v_med3_f32 v5, v46, s70, v164
	v_med3_f32 v46, v42, s70, v164
	v_med3_f32 v47, v47, s70, v164
	v_mov_b32_e32 v42, v147
	v_cvt_pk_fp8_f32 v42, v5, v47
	v_pk_fma_f32 v[48:49], v[48:49], s[36:37], v[8:9] op_sel_hi:[1,0,1]
	v_mov_b32_e32 v51, v147
	v_pk_mul_f32 v[48:49], v[64:65], v[48:49] op_sel_hi:[0,1]
	v_med3_f32 v48, v48, s70, v164
	v_med3_f32 v5, v49, s70, v164
	v_cvt_pk_fp8_f32 v42, v48, v5 op_sel:[0,0,1]
	v_mul_f32_e32 v48, 0x41000000, v165
	v_pk_fma_f32 v[38:39], v[38:39], s[36:37], v[158:159] op_sel_hi:[1,0,1]
	v_pk_fma_f32 v[34:35], v[34:35], s[36:37], v[154:155] op_sel_hi:[1,0,1]
	v_cvt_pk_fp8_f32 v51, v54, v65
	v_pk_mul_f32 v[38:39], v[48:49], v[38:39] op_sel_hi:[0,1]
	v_pk_mul_f32 v[34:35], v[48:49], v[34:35] op_sel_hi:[0,1]
	v_med3_f32 v5, v38, s70, v164
	v_med3_f32 v38, v34, s70, v164
	v_med3_f32 v39, v39, s70, v164
	v_mov_b32_e32 v34, v147
	v_cvt_pk_fp8_f32 v34, v5, v39
	v_med3_f32 v52, v52, s70, v164
	v_med3_f32 v53, v53, s70, v164
	v_pk_fma_f32 v[40:41], v[40:41], s[36:37], v[156:157] op_sel_hi:[1,0,1]
	v_pk_fma_f32 v[36:37], v[36:37], s[36:37], v[152:153] op_sel_hi:[1,0,1]
	v_cvt_pk_fp8_f32 v51, v52, v53 op_sel:[0,0,1]
	v_med3_f32 v52, v43, s70, v164
	v_mov_b32_e32 v43, v147
	v_pk_mul_f32 v[40:41], v[48:49], v[40:41] op_sel_hi:[0,1]
	v_pk_mul_f32 v[36:37], v[48:49], v[36:37] op_sel_hi:[0,1]
	v_med3_f32 v49, v35, s70, v164
	v_pk_fma_f32 v[30:31], v[30:31], s[36:37], v[150:151] op_sel_hi:[1,0,1]
	v_pk_fma_f32 v[26:27], v[26:27], s[36:37], v[6:7] op_sel_hi:[1,0,1]
	v_cvt_pk_fp8_f32 v43, v46, v52
	v_med3_f32 v40, v40, s70, v164
	v_med3_f32 v5, v41, s70, v164
	v_pk_mul_f32 v[30:31], v[48:49], v[30:31] op_sel_hi:[0,1]
	v_pk_mul_f32 v[26:27], v[48:49], v[26:27] op_sel_hi:[0,1]
	v_add_u32_e32 v62, 0x80, v4
	v_pk_fma_f32 v[44:45], v[44:45], s[36:37], v[2:3] op_sel_hi:[1,0,1]
	v_mov_b32_e32 v35, v147
	v_cvt_pk_fp8_f32 v34, v40, v5 op_sel:[0,0,1]
	v_med3_f32 v5, v30, s70, v164
	v_med3_f32 v30, v26, s70, v164
	v_med3_f32 v31, v31, s70, v164
	v_mov_b32_e32 v26, v147
	ds_read_b128 v[58:61], v123
	v_ashrrev_i32_e32 v63, 31, v62
	v_pk_mul_f32 v[44:45], v[64:65], v[44:45] op_sel_hi:[0,1]
	v_cvt_pk_fp8_f32 v35, v38, v49
	v_cvt_pk_fp8_f32 v26, v5, v31
	v_lshlrev_b64 v[62:63], 10, v[62:63]
	v_med3_f32 v44, v44, s70, v164
	v_med3_f32 v45, v45, s70, v164
	v_pk_fma_f32 v[32:33], v[32:33], s[36:37], v[8:9] op_sel_hi:[1,0,1]
	v_lshl_add_u64 v[62:63], s[16:17], 0, v[62:63]
	v_cvt_pk_fp8_f32 v43, v44, v45 op_sel:[0,0,1]
	v_pk_mul_f32 v[32:33], v[48:49], v[32:33] op_sel_hi:[0,1]
	v_lshl_add_u64 v[62:63], v[62:63], 0, s[6:7]
	v_med3_f32 v36, v36, s70, v164
	v_med3_f32 v37, v37, s70, v164
	v_med3_f32 v32, v32, s70, v164
	v_med3_f32 v5, v33, s70, v164
	v_lshl_add_u64 v[44:45], v[62:63], 0, v[146:147]
	v_cvt_pk_fp8_f32 v35, v36, v37 op_sel:[0,0,1]
	v_med3_f32 v36, v27, s70, v164
	v_mov_b32_e32 v27, v147
	v_cvt_pk_fp8_f32 v26, v32, v5 op_sel:[0,0,1]
	v_mul_f32_e32 v32, 0x41000000, v1
	v_pk_fma_f32 v[22:23], v[22:23], s[36:37], v[158:159] op_sel_hi:[1,0,1]
	v_pk_fma_f32 v[18:19], v[18:19], s[36:37], v[154:155] op_sel_hi:[1,0,1]
	s_waitcnt lgkmcnt(0)
	global_store_dwordx4 v[44:45], v[58:61], off
	v_cvt_pk_fp8_f32 v27, v30, v36
	v_pk_mul_f32 v[22:23], v[32:33], v[22:23] op_sel_hi:[0,1]
	v_pk_mul_f32 v[18:19], v[32:33], v[18:19] op_sel_hi:[0,1]
	ds_write2_b64 v122, v[50:51], v[42:43] offset1:4
	v_add_u32_e32 v46, 0x90, v4
	v_pk_fma_f32 v[28:29], v[28:29], s[36:37], v[2:3] op_sel_hi:[1,0,1]
	v_med3_f32 v1, v22, s70, v164
	v_med3_f32 v5, v18, s70, v164
	v_med3_f32 v22, v23, s70, v164
	v_med3_f32 v23, v19, s70, v164
	v_mov_b32_e32 v18, v147
	v_mov_b32_e32 v19, v147
	ds_read_b128 v[42:45], v123
	v_ashrrev_i32_e32 v47, 31, v46
	v_pk_mul_f32 v[28:29], v[48:49], v[28:29] op_sel_hi:[0,1]
	v_cvt_pk_fp8_f32 v18, v1, v22
	v_cvt_pk_fp8_f32 v19, v5, v23
	v_lshlrev_b64 v[46:47], 10, v[46:47]
	v_med3_f32 v28, v28, s70, v164
	v_med3_f32 v29, v29, s70, v164
	v_pk_fma_f32 v[24:25], v[24:25], s[36:37], v[156:157] op_sel_hi:[1,0,1]
	v_pk_fma_f32 v[20:21], v[20:21], s[36:37], v[152:153] op_sel_hi:[1,0,1]
	v_lshl_add_u64 v[46:47], s[16:17], 0, v[46:47]
	v_cvt_pk_fp8_f32 v27, v28, v29 op_sel:[0,0,1]
	v_pk_mul_f32 v[24:25], v[32:33], v[24:25] op_sel_hi:[0,1]
	v_pk_mul_f32 v[20:21], v[32:33], v[20:21] op_sel_hi:[0,1]
	v_pk_fma_f32 v[14:15], v[14:15], s[36:37], v[150:151] op_sel_hi:[1,0,1]
	v_pk_fma_f32 v[6:7], v[10:11], s[36:37], v[6:7] op_sel_hi:[1,0,1]
	v_lshl_add_u64 v[46:47], v[46:47], 0, s[6:7]
	v_med3_f32 v24, v24, s70, v164
	v_med3_f32 v20, v20, s70, v164
	v_med3_f32 v1, v25, s70, v164
	v_med3_f32 v5, v21, s70, v164
	v_pk_mul_f32 v[14:15], v[32:33], v[14:15] op_sel_hi:[0,1]
	v_pk_mul_f32 v[6:7], v[32:33], v[6:7] op_sel_hi:[0,1]
	v_lshl_add_u64 v[28:29], v[46:47], 0, v[146:147]
	v_cvt_pk_fp8_f32 v18, v24, v1 op_sel:[0,0,1]
	v_cvt_pk_fp8_f32 v19, v20, v5 op_sel:[0,0,1]
	v_med3_f32 v1, v14, s70, v164
	v_med3_f32 v5, v6, s70, v164
	v_med3_f32 v10, v15, s70, v164
	v_med3_f32 v11, v7, s70, v164
	v_mov_b32_e32 v6, v147
	v_mov_b32_e32 v7, v147
	s_waitcnt lgkmcnt(0)
	global_store_dwordx4 v[28:29], v[42:45], off
	v_cvt_pk_fp8_f32 v6, v1, v10
	v_cvt_pk_fp8_f32 v7, v5, v11
	ds_write2_b64 v122, v[34:35], v[26:27] offset1:4
	v_add_u32_e32 v30, 0xa0, v4
	v_pk_fma_f32 v[8:9], v[16:17], s[36:37], v[8:9] op_sel_hi:[1,0,1]
	v_pk_fma_f32 v[2:3], v[12:13], s[36:37], v[2:3] op_sel_hi:[1,0,1]
	ds_read_b128 v[26:29], v123
	v_ashrrev_i32_e32 v31, 31, v30
	v_pk_mul_f32 v[8:9], v[32:33], v[8:9] op_sel_hi:[0,1]
	v_pk_mul_f32 v[2:3], v[32:33], v[2:3] op_sel_hi:[0,1]
	v_lshlrev_b64 v[30:31], 10, v[30:31]
	v_med3_f32 v8, v8, s70, v164
	v_med3_f32 v2, v2, s70, v164
	v_med3_f32 v1, v9, s70, v164
	v_med3_f32 v3, v3, s70, v164
	v_lshl_add_u64 v[30:31], s[16:17], 0, v[30:31]
	v_cvt_pk_fp8_f32 v6, v8, v1 op_sel:[0,0,1]
	v_cvt_pk_fp8_f32 v7, v2, v3 op_sel:[0,0,1]
	v_lshl_add_u64 v[30:31], v[30:31], 0, s[6:7]
	v_lshl_add_u64 v[2:3], v[30:31], 0, v[146:147]
	s_waitcnt lgkmcnt(0)
	global_store_dwordx4 v[2:3], v[26:29], off
	ds_write2_b64 v122, v[18:19], v[6:7] offset1:4
	v_add_u32_e32 v2, 0xb0, v4
	ds_read_b128 v[6:9], v123
	v_ashrrev_i32_e32 v3, 31, v2
	v_lshlrev_b64 v[2:3], 10, v[2:3]
	v_lshl_add_u64 v[2:3], s[16:17], 0, v[2:3]
	v_lshl_add_u64 v[2:3], v[2:3], 0, s[6:7]
	v_lshl_add_u64 v[2:3], v[2:3], 0, v[146:147]
	s_waitcnt lgkmcnt(0)
	global_store_dwordx4 v[2:3], v[6:9], off
	s_and_b64 vcc, exec, s[8:9]
	s_mov_b64 s[6:7], -1
	s_cbranch_vccnz .LBB0_1616
	v_mov_b32_e32 v12, v0
	s_lshl_b32 s7, s40, 8
	v_readfirstlane_b32 s6, v12
	s_and_b32 s8, s6, 0xc0
	s_ashr_i32 s6, s6, 2
	s_andn2_b32 s6, s6, 63
	s_add_i32 s6, s6, s7
	v_and_or_b32 v2, v12, 15, s6
	v_ashrrev_i32_e32 v3, 31, v2
	s_lshl_b64 s[6:7], s[42:43], 11
	v_lshl_add_u64 v[4:5], v[2:3], 2, s[12:13]
	v_add_u32_e32 v6, 0x80, v2
	v_add_u32_e32 v8, 0x90, v2
	v_add_u32_e32 v10, 0xa0, v2
	v_add_u32_e32 v2, 0xb0, v2
	s_add_u32 s9, s56, s6
	v_ashrrev_i32_e32 v7, 31, v6
	v_ashrrev_i32_e32 v9, 31, v8
	v_ashrrev_i32_e32 v11, 31, v10
	v_ashrrev_i32_e32 v3, 31, v2
	s_addc_u32 s39, s57, s7
	s_lshl_b32 s6, s38, 8
	v_lshl_add_u64 v[6:7], v[6:7], 2, s[12:13]
	v_lshl_add_u64 v[8:9], v[8:9], 2, s[12:13]
	v_lshl_add_u64 v[10:11], v[10:11], 2, s[12:13]
	v_lshl_add_u64 v[2:3], v[2:3], 2, s[12:13]
	global_load_dword v146, v[4:5], off
	global_load_dword v170, v[4:5], off offset:64
	global_load_dword v169, v[4:5], off offset:128
	global_load_dword v168, v[4:5], off offset:192
	global_load_dword v167, v[6:7], off
	global_load_dword v166, v[8:9], off
	global_load_dword v165, v[10:11], off
	global_load_dword v1, v[2:3], off
	s_ashr_i32 s7, s6, 31
	s_lshl_b64 s[6:7], s[6:7], 1
	s_add_u32 s6, s9, s6
	s_addc_u32 s7, s39, s7
	s_lshl_b32 s8, s8, 1
	s_add_u32 s6, s6, s8
	s_addc_u32 s7, s7, 0
	v_and_b32_e32 v2, 48, v12
	global_load_dwordx4 v[6:9], v2, s[6:7]
	s_nop 0
	global_load_dwordx4 v[2:5], v2, s[6:7] offset:64
	s_andn2_b64 vcc, exec, s[14:15]
	s_cbranch_vccnz .LBB0_1615
	s_barrier
	s_branch .LBB0_1615

.LBB0_3348:
	v_lshlrev_b32_e32 v160, 16, v46
	v_and_b32_e32 v161, 0xffff0000, v46
	v_lshlrev_b32_e32 v156, 16, v42
	v_and_b32_e32 v157, 0xffff0000, v42
	v_mul_f32_e32 v42, 0x3d800000, v179
	v_lshlrev_b32_e32 v154, 16, v47
	v_and_b32_e32 v155, 0xffff0000, v47
	v_lshlrev_b32_e32 v46, 16, v44
	v_and_b32_e32 v47, 0xffff0000, v44
	v_lshlrev_b32_e32 v150, 16, v45
	v_and_b32_e32 v151, 0xffff0000, v45
	v_pk_fma_f32 v[44:45], v[42:43], v[130:131], v[160:161] op_sel_hi:[0,1,1]
	v_min_f32_e32 v44, 0x41898193, v44
	v_min_f32_e32 v45, 0x41898193, v45
	v_exp_f32_e64 v130, -v44
	v_exp_f32_e64 v131, -v45
	v_pk_fma_f32 v[132:133], v[42:43], v[132:133], v[154:155] op_sel_hi:[0,1,1]
	v_min_f32_e32 v132, 0x41898193, v132
	v_min_f32_e32 v133, 0x41898193, v133
	v_pk_add_f32 v[130:131], v[130:131], 1.0 op_sel_hi:[1,0]
	v_exp_f32_e64 v180, -v132
	v_rcp_f32_e32 v130, v130
	v_rcp_f32_e32 v131, v131
	v_exp_f32_e64 v181, -v133
	v_lshlrev_b32_e32 v152, 16, v48
	v_and_b32_e32 v153, 0xffff0000, v48
	v_pk_mul_f32 v[44:45], v[44:45], v[130:131]
	v_pk_add_f32 v[130:131], v[180:181], 1.0 op_sel_hi:[1,0]
	v_pk_fma_f32 v[122:123], v[42:43], v[122:123], v[152:153] op_sel_hi:[0,1,1]
	v_rcp_f32_e32 v130, v130
	v_rcp_f32_e32 v131, v131
	v_min_f32_e32 v122, 0x41898193, v122
	v_min_f32_e32 v123, 0x41898193, v123
	v_lshlrev_b32_e32 v48, 16, v49
	v_pk_mul_f32 v[130:131], v[132:133], v[130:131]
	v_exp_f32_e64 v132, -v122
	v_exp_f32_e64 v133, -v123
	v_and_b32_e32 v49, 0xffff0000, v49
	v_pk_fma_f32 v[124:125], v[42:43], v[124:125], v[48:49] op_sel_hi:[0,1,1]
	v_lshlrev_b32_e32 v158, 16, v43
	v_and_b32_e32 v159, 0xffff0000, v43
	v_min_f32_e32 v124, 0x41898193, v124
	v_min_f32_e32 v125, 0x41898193, v125
	v_pk_fma_f32 v[136:137], v[42:43], v[136:137], v[158:159] op_sel_hi:[0,1,1]
	v_pk_fma_f32 v[134:135], v[42:43], v[134:135], v[156:157] op_sel_hi:[0,1,1]
	v_pk_fma_f32 v[128:129], v[42:43], v[128:129], v[150:151] op_sel_hi:[0,1,1]
	v_pk_add_f32 v[132:133], v[132:133], 1.0 op_sel_hi:[1,0]
	v_pk_fma_f32 v[42:43], v[42:43], v[126:127], v[46:47] op_sel_hi:[0,1,1]
	v_exp_f32_e64 v126, -v124
	v_exp_f32_e64 v127, -v125
	v_rcp_f32_e32 v132, v132
	v_rcp_f32_e32 v133, v133
	v_med3_f32 v42, v42, s81, v170
	v_pk_add_f32 v[126:127], v[126:127], 1.0 op_sel_hi:[1,0]
	v_med3_f32 v43, v43, s81, v170
	v_pk_mul_f32 v[122:123], v[122:123], v[132:133]
	v_rcp_f32_e32 v126, v126
	v_rcp_f32_e32 v127, v127
	v_pk_mul_f32 v[42:43], v[122:123], v[42:43]
	v_med3_f32 v123, v129, s81, v170
	v_mov_b32_e32 v129, 0
	v_cvt_pk_fp8_f32 v129, v42, v43
	v_med3_f32 v122, v128, s81, v170
	v_pk_mul_f32 v[42:43], v[124:125], v[126:127]
	v_med3_f32 v134, v134, s81, v170
	v_med3_f32 v135, v135, s81, v170
	v_pk_mul_f32 v[42:43], v[42:43], v[122:123]
	v_pk_mul_f32 v[44:45], v[44:45], v[134:135]
	v_mov_b32_e32 v128, 0
	v_cvt_pk_fp8_f32 v129, v42, v43 op_sel:[0,0,1]
	v_mul_f32_e32 v42, 0x3d800000, v178
	v_cvt_pk_fp8_f32 v128, v44, v45
	v_pk_fma_f32 v[44:45], v[42:43], v[114:115], v[160:161] op_sel_hi:[0,1,1]
	v_min_f32_e32 v44, 0x41898193, v44
	v_min_f32_e32 v45, 0x41898193, v45
	v_exp_f32_e64 v114, -v44
	v_exp_f32_e64 v115, -v45
	v_pk_fma_f32 v[116:117], v[42:43], v[116:117], v[154:155] op_sel_hi:[0,1,1]
	v_min_f32_e32 v116, 0x41898193, v116
	v_min_f32_e32 v117, 0x41898193, v117
	v_pk_add_f32 v[114:115], v[114:115], 1.0 op_sel_hi:[1,0]
	v_exp_f32_e64 v122, -v116
	v_rcp_f32_e32 v114, v114
	v_rcp_f32_e32 v115, v115
	v_exp_f32_e64 v123, -v117
	v_pk_fma_f32 v[106:107], v[42:43], v[106:107], v[152:153] op_sel_hi:[0,1,1]
	v_min_f32_e32 v106, 0x41898193, v106
	v_pk_mul_f32 v[44:45], v[44:45], v[114:115]
	v_pk_add_f32 v[114:115], v[122:123], 1.0 op_sel_hi:[1,0]
	v_min_f32_e32 v107, 0x41898193, v107
	v_rcp_f32_e32 v114, v114
	v_rcp_f32_e32 v115, v115
	v_pk_fma_f32 v[108:109], v[42:43], v[108:109], v[48:49] op_sel_hi:[0,1,1]
	v_min_f32_e32 v108, 0x41898193, v108
	v_min_f32_e32 v109, 0x41898193, v109
	v_pk_mul_f32 v[114:115], v[116:117], v[114:115]
	v_exp_f32_e64 v116, -v106
	v_exp_f32_e64 v117, -v107
	v_pk_fma_f32 v[120:121], v[42:43], v[120:121], v[158:159] op_sel_hi:[0,1,1]
	v_pk_fma_f32 v[118:119], v[42:43], v[118:119], v[156:157] op_sel_hi:[0,1,1]
	v_pk_fma_f32 v[112:113], v[42:43], v[112:113], v[150:151] op_sel_hi:[0,1,1]
	v_pk_add_f32 v[116:117], v[116:117], 1.0 op_sel_hi:[1,0]
	v_pk_fma_f32 v[42:43], v[42:43], v[110:111], v[46:47] op_sel_hi:[0,1,1]
	v_exp_f32_e64 v110, -v108
	v_exp_f32_e64 v111, -v109
	v_rcp_f32_e32 v116, v116
	v_rcp_f32_e32 v117, v117
	v_med3_f32 v118, v118, s81, v170
	v_pk_add_f32 v[110:111], v[110:111], 1.0 op_sel_hi:[1,0]
	v_med3_f32 v119, v119, s81, v170
	v_med3_f32 v42, v42, s81, v170
	v_med3_f32 v43, v43, s81, v170
	v_pk_mul_f32 v[106:107], v[106:107], v[116:117]
	v_rcp_f32_e32 v110, v110
	v_rcp_f32_e32 v111, v111
	v_pk_mul_f32 v[44:45], v[44:45], v[118:119]
	v_pk_mul_f32 v[42:43], v[106:107], v[42:43]
	v_med3_f32 v106, v112, s81, v170
	v_med3_f32 v107, v113, s81, v170
	v_mov_b32_e32 v112, 0
	v_mov_b32_e32 v113, 0
	v_mov_b32_e32 v142, v0
	v_cvt_pk_fp8_f32 v112, v44, v45
	v_cvt_pk_fp8_f32 v113, v42, v43
	v_med3_f32 v134, v136, s81, v170
	v_readfirstlane_b32 s65, v142
	v_med3_f32 v135, v137, s81, v170
	s_ashr_i32 s10, s65, 6
	v_pk_mul_f32 v[130:131], v[130:131], v[134:135]
	v_med3_f32 v118, v120, s81, v170
	v_med3_f32 v119, v121, s81, v170
	v_pk_mul_f32 v[42:43], v[108:109], v[110:111]
	s_mul_i32 s11, s10, 0xb00
	v_cvt_pk_fp8_f32 v128, v130, v131 op_sel:[0,0,1]
	v_pk_mul_f32 v[114:115], v[114:115], v[118:119]
	v_pk_mul_f32 v[42:43], v[42:43], v[106:107]
	s_add_i32 s67, s11, 0
	v_and_b32_e32 v147, 15, v142
	v_lshrrev_b32_e32 v125, 1, v142
	v_cvt_pk_fp8_f32 v112, v114, v115 op_sel:[0,0,1]
	v_cvt_pk_fp8_f32 v113, v42, v43 op_sel:[0,0,1]
	s_add_i32 s67, s67, 0x20000
	v_mul_u32_u24_e32 v124, 48, v147
	v_and_b32_e32 v42, 24, v125
	v_add3_u32 v108, s67, v124, v42
	ds_write_b64 v108, v[128:129]
	ds_write_b64 v108, v[112:113] offset:768
	s_cmp_lg_u64 s[28:29], 0
	s_cbranch_scc0 .Lepibar_gu1
	s_barrier
.Lepibar_gu1:
	v_mul_f32_e32 v112, 0x3d800000, v177
	v_pk_fma_f32 v[98:99], v[112:113], v[98:99], v[160:161] op_sel_hi:[0,1,1]
	v_min_f32_e32 v98, 0x41898193, v98
	v_min_f32_e32 v99, 0x41898193, v99
	v_exp_f32_e64 v114, -v98
	v_exp_f32_e64 v115, -v99
	v_pk_fma_f32 v[100:101], v[112:113], v[100:101], v[154:155] op_sel_hi:[0,1,1]
	v_min_f32_e32 v100, 0x41898193, v100
	v_min_f32_e32 v101, 0x41898193, v101
	v_pk_add_f32 v[114:115], v[114:115], 1.0 op_sel_hi:[1,0]
	v_exp_f32_e64 v116, -v100
	v_rcp_f32_e32 v114, v114
	v_rcp_f32_e32 v115, v115
	v_exp_f32_e64 v117, -v101
	v_pk_fma_f32 v[102:103], v[112:113], v[102:103], v[156:157] op_sel_hi:[0,1,1]
	v_pk_fma_f32 v[90:91], v[112:113], v[90:91], v[152:153] op_sel_hi:[0,1,1]
	v_pk_mul_f32 v[98:99], v[98:99], v[114:115]
	v_pk_add_f32 v[114:115], v[116:117], 1.0 op_sel_hi:[1,0]
	v_pk_fma_f32 v[104:105], v[112:113], v[104:105], v[158:159] op_sel_hi:[0,1,1]
	v_med3_f32 v102, v102, s81, v170
	v_med3_f32 v103, v103, s81, v170
	v_rcp_f32_e32 v114, v114
	v_rcp_f32_e32 v115, v115
	v_min_f32_e32 v90, 0x41898193, v90
	v_min_f32_e32 v91, 0x41898193, v91
	v_pk_mul_f32 v[98:99], v[98:99], v[102:103]
	v_med3_f32 v102, v104, s81, v170
	v_med3_f32 v103, v105, s81, v170
	v_exp_f32_e64 v104, -v90
	v_exp_f32_e64 v105, -v91
	v_pk_mul_f32 v[100:101], v[100:101], v[114:115]
	v_pk_fma_f32 v[92:93], v[112:113], v[92:93], v[48:49] op_sel_hi:[0,1,1]
	v_pk_mul_f32 v[100:101], v[100:101], v[102:103]
	v_pk_add_f32 v[102:103], v[104:105], 1.0 op_sel_hi:[1,0]
	v_min_f32_e32 v92, 0x41898193, v92
	v_rcp_f32_e32 v102, v102
	v_rcp_f32_e32 v103, v103
	v_min_f32_e32 v93, 0x41898193, v93
	v_pk_fma_f32 v[94:95], v[112:113], v[94:95], v[46:47] op_sel_hi:[0,1,1]
	v_pk_fma_f32 v[96:97], v[112:113], v[96:97], v[150:151] op_sel_hi:[0,1,1]
	v_pk_mul_f32 v[90:91], v[90:91], v[102:103]
	v_exp_f32_e64 v102, -v92
	v_exp_f32_e64 v103, -v93
	v_med3_f32 v94, v94, s81, v170
	v_med3_f32 v95, v95, s81, v170
	v_pk_mul_f32 v[90:91], v[90:91], v[94:95]
	v_med3_f32 v94, v96, s81, v170
	v_med3_f32 v95, v97, s81, v170
	v_pk_add_f32 v[96:97], v[102:103], 1.0 op_sel_hi:[1,0]
	v_mov_b32_e32 v103, v143
	v_rcp_f32_e32 v96, v96
	v_rcp_f32_e32 v97, v97
	v_cvt_pk_fp8_f32 v103, v90, v91
	v_mov_b32_e32 v102, v143
	v_bfe_u32 v106, v142, 1, 5
	v_pk_mul_f32 v[90:91], v[92:93], v[96:97]
	v_lshlrev_b32_e32 v43, 4, v142
	v_pk_mul_f32 v[90:91], v[90:91], v[94:95]
	s_ashr_i32 s65, s65, 2
	v_cvt_pk_fp8_f32 v103, v90, v91 op_sel:[0,0,1]
	v_mul_f32_e32 v90, 0x3d800000, v176
	v_pk_fma_f32 v[82:83], v[90:91], v[82:83], v[160:161] op_sel_hi:[0,1,1]
	v_min_f32_e32 v82, 0x41898193, v82
	v_min_f32_e32 v83, 0x41898193, v83
	v_exp_f32_e64 v92, -v82
	v_exp_f32_e64 v93, -v83
	v_pk_fma_f32 v[84:85], v[90:91], v[84:85], v[154:155] op_sel_hi:[0,1,1]
	v_min_f32_e32 v84, 0x41898193, v84
	v_min_f32_e32 v85, 0x41898193, v85
	v_pk_add_f32 v[92:93], v[92:93], 1.0 op_sel_hi:[1,0]
	v_exp_f32_e64 v94, -v84
	v_rcp_f32_e32 v92, v92
	v_rcp_f32_e32 v93, v93
	v_exp_f32_e64 v95, -v85
	v_pk_fma_f32 v[86:87], v[90:91], v[86:87], v[156:157] op_sel_hi:[0,1,1]
	v_pk_fma_f32 v[66:67], v[90:91], v[66:67], v[152:153] op_sel_hi:[0,1,1]
	v_pk_mul_f32 v[82:83], v[82:83], v[92:93]
	v_pk_add_f32 v[92:93], v[94:95], 1.0 op_sel_hi:[1,0]
	v_pk_fma_f32 v[88:89], v[90:91], v[88:89], v[158:159] op_sel_hi:[0,1,1]
	v_med3_f32 v86, v86, s81, v170
	v_med3_f32 v87, v87, s81, v170
	v_rcp_f32_e32 v92, v92
	v_rcp_f32_e32 v93, v93
	v_min_f32_e32 v66, 0x41898193, v66
	v_min_f32_e32 v67, 0x41898193, v67
	v_pk_mul_f32 v[82:83], v[82:83], v[86:87]
	v_med3_f32 v86, v88, s81, v170
	v_med3_f32 v87, v89, s81, v170
	v_exp_f32_e64 v88, -v66
	v_exp_f32_e64 v89, -v67
	v_pk_mul_f32 v[84:85], v[84:85], v[92:93]
	v_pk_fma_f32 v[68:69], v[90:91], v[68:69], v[48:49] op_sel_hi:[0,1,1]
	v_pk_mul_f32 v[84:85], v[84:85], v[86:87]
	v_pk_add_f32 v[86:87], v[88:89], 1.0 op_sel_hi:[1,0]
	v_min_f32_e32 v68, 0x41898193, v68
	v_rcp_f32_e32 v86, v86
	v_rcp_f32_e32 v87, v87
	v_min_f32_e32 v69, 0x41898193, v69
	v_pk_fma_f32 v[74:75], v[90:91], v[74:75], v[46:47] op_sel_hi:[0,1,1]
	v_pk_fma_f32 v[76:77], v[90:91], v[76:77], v[150:151] op_sel_hi:[0,1,1]
	v_pk_mul_f32 v[66:67], v[66:67], v[86:87]
	v_exp_f32_e64 v86, -v68
	v_exp_f32_e64 v87, -v69
	v_med3_f32 v74, v74, s81, v170
	v_med3_f32 v75, v75, s81, v170
	v_pk_mul_f32 v[66:67], v[66:67], v[74:75]
	v_med3_f32 v74, v76, s81, v170
	v_med3_f32 v75, v77, s81, v170
	v_pk_add_f32 v[76:77], v[86:87], 1.0 op_sel_hi:[1,0]
	v_mov_b32_e32 v87, v143
	v_rcp_f32_e32 v76, v76
	v_rcp_f32_e32 v77, v77
	v_cvt_pk_fp8_f32 v87, v66, v67
	v_cvt_pk_fp8_f32 v102, v98, v99
	v_mov_b32_e32 v86, v143
	v_pk_mul_f32 v[66:67], v[68:69], v[76:77]
	v_mul_f32_e32 v68, 0x3d800000, v175
	v_pk_fma_f32 v[70:71], v[68:69], v[70:71], v[160:161] op_sel_hi:[0,1,1]
	v_min_f32_e32 v70, 0x41898193, v70
	v_min_f32_e32 v71, 0x41898193, v71
	v_pk_mul_f32 v[66:67], v[66:67], v[74:75]
	v_exp_f32_e64 v74, -v70
	v_exp_f32_e64 v75, -v71
	v_pk_fma_f32 v[72:73], v[68:69], v[72:73], v[154:155] op_sel_hi:[0,1,1]
	v_min_f32_e32 v72, 0x41898193, v72
	v_min_f32_e32 v73, 0x41898193, v73
	v_pk_add_f32 v[74:75], v[74:75], 1.0 op_sel_hi:[1,0]
	v_pk_fma_f32 v[76:77], v[68:69], v[80:81], v[158:159] op_sel_hi:[0,1,1]
	v_rcp_f32_e32 v74, v74
	v_rcp_f32_e32 v75, v75
	v_exp_f32_e64 v80, -v72
	v_exp_f32_e64 v81, -v73
	v_pk_fma_f32 v[58:59], v[68:69], v[58:59], v[152:153] op_sel_hi:[0,1,1]
	v_pk_mul_f32 v[70:71], v[70:71], v[74:75]
	v_min_f32_e32 v58, 0x41898193, v58
	v_pk_add_f32 v[74:75], v[80:81], 1.0 op_sel_hi:[1,0]
	v_min_f32_e32 v59, 0x41898193, v59
	v_rcp_f32_e32 v74, v74
	v_rcp_f32_e32 v75, v75
	v_pk_fma_f32 v[60:61], v[68:69], v[60:61], v[48:49] op_sel_hi:[0,1,1]
	v_min_f32_e32 v60, 0x41898193, v60
	v_min_f32_e32 v61, 0x41898193, v61
	v_pk_mul_f32 v[72:73], v[72:73], v[74:75]
	v_exp_f32_e64 v74, -v58
	v_exp_f32_e64 v75, -v59
	v_pk_fma_f32 v[78:79], v[68:69], v[78:79], v[156:157] op_sel_hi:[0,1,1]
	v_pk_fma_f32 v[64:65], v[68:69], v[64:65], v[150:151] op_sel_hi:[0,1,1]
	v_pk_fma_f32 v[62:63], v[68:69], v[62:63], v[46:47] op_sel_hi:[0,1,1]
	v_pk_add_f32 v[74:75], v[74:75], 1.0 op_sel_hi:[1,0]
	v_exp_f32_e64 v68, -v60
	v_rcp_f32_e32 v74, v74
	v_rcp_f32_e32 v75, v75
	v_exp_f32_e64 v69, -v61
	v_med3_f32 v62, v62, s81, v170
	v_med3_f32 v63, v63, s81, v170
	v_pk_mul_f32 v[58:59], v[58:59], v[74:75]
	v_mul_u32_u24_e32 v42, 48, v106
	v_pk_mul_f32 v[58:59], v[58:59], v[62:63]
	v_med3_f32 v62, v64, s81, v170
	v_med3_f32 v63, v65, s81, v170
	v_pk_add_f32 v[64:65], v[68:69], 1.0 op_sel_hi:[1,0]
	v_mov_b32_e32 v69, v143
	v_rcp_f32_e32 v64, v64
	v_rcp_f32_e32 v65, v65
	v_cvt_pk_fp8_f32 v69, v58, v59
	v_and_b32_e32 v142, 16, v43
	s_andn2_b32 s65, s65, 63
	v_pk_mul_f32 v[58:59], v[60:61], v[64:65]
	v_lshl_or_b32 v106, s74, 8, v106
	v_pk_mul_f32 v[58:59], v[58:59], v[62:63]
	v_cvt_pk_fp8_f32 v86, v82, v83
	v_cvt_pk_fp8_f32 v69, v58, v59 op_sel:[0,0,1]
	v_mul_f32_e32 v58, 0x3d800000, v174
	v_pk_fma_f32 v[50:51], v[58:59], v[50:51], v[160:161] op_sel_hi:[0,1,1]
	v_min_f32_e32 v50, 0x41898193, v50
	v_min_f32_e32 v51, 0x41898193, v51
	v_exp_f32_e64 v60, -v50
	v_exp_f32_e64 v61, -v51
	v_pk_fma_f32 v[52:53], v[58:59], v[52:53], v[154:155] op_sel_hi:[0,1,1]
	v_min_f32_e32 v52, 0x41898193, v52
	v_min_f32_e32 v53, 0x41898193, v53
	v_pk_add_f32 v[60:61], v[60:61], 1.0 op_sel_hi:[1,0]
	v_exp_f32_e64 v62, -v52
	v_rcp_f32_e32 v60, v60
	v_rcp_f32_e32 v61, v61
	v_exp_f32_e64 v63, -v53
	v_pk_fma_f32 v[54:55], v[58:59], v[54:55], v[156:157] op_sel_hi:[0,1,1]
	v_pk_fma_f32 v[34:35], v[58:59], v[34:35], v[152:153] op_sel_hi:[0,1,1]
	v_pk_mul_f32 v[50:51], v[50:51], v[60:61]
	v_pk_add_f32 v[60:61], v[62:63], 1.0 op_sel_hi:[1,0]
	v_pk_fma_f32 v[56:57], v[58:59], v[56:57], v[158:159] op_sel_hi:[0,1,1]
	v_med3_f32 v54, v54, s81, v170
	v_med3_f32 v55, v55, s81, v170
	v_rcp_f32_e32 v60, v60
	v_rcp_f32_e32 v61, v61
	v_min_f32_e32 v34, 0x41898193, v34
	v_min_f32_e32 v35, 0x41898193, v35
	v_pk_mul_f32 v[50:51], v[50:51], v[54:55]
	v_med3_f32 v54, v56, s81, v170
	v_med3_f32 v55, v57, s81, v170
	v_exp_f32_e64 v56, -v34
	v_exp_f32_e64 v57, -v35
	v_pk_mul_f32 v[52:53], v[52:53], v[60:61]
	v_pk_fma_f32 v[36:37], v[58:59], v[36:37], v[48:49] op_sel_hi:[0,1,1]
	v_pk_mul_f32 v[52:53], v[52:53], v[54:55]
	v_pk_add_f32 v[54:55], v[56:57], 1.0 op_sel_hi:[1,0]
	v_min_f32_e32 v36, 0x41898193, v36
	v_rcp_f32_e32 v54, v54
	v_rcp_f32_e32 v55, v55
	v_min_f32_e32 v37, 0x41898193, v37
	s_lshl_b32 s10, s10, 5
	v_add3_u32 v109, s67, v42, v142
	v_add_u32_e32 v106, s65, v106
	v_pk_mul_f32 v[34:35], v[34:35], v[54:55]
	v_exp_f32_e64 v54, -v36
	v_exp_f32_e64 v55, -v37
	s_lshl_b32 s11, s76, 7
	s_and_b32 s10, s10, 0x60
	ds_read_b128 v[42:45], v109
	v_ashrrev_i32_e32 v107, 31, v106
	s_or_b32 s10, s10, s11
	v_lshlrev_b64 v[110:111], 10, v[106:107]
	v_cvt_pk_fp8_f32 v102, v100, v101 op_sel:[0,0,1]
	v_pk_fma_f32 v[38:39], v[58:59], v[38:39], v[46:47] op_sel_hi:[0,1,1]
	s_ashr_i32 s11, s10, 31
	v_lshl_add_u64 v[110:111], s[18:19], 0, v[110:111]
	v_cvt_pk_fp8_f32 v86, v84, v85 op_sel:[0,0,1]
	v_cvt_pk_fp8_f32 v87, v66, v67 op_sel:[0,0,1]
	v_pk_fma_f32 v[40:41], v[58:59], v[40:41], v[150:151] op_sel_hi:[0,1,1]
	v_med3_f32 v38, v38, s81, v170
	v_med3_f32 v39, v39, s81, v170
	v_lshl_add_u64 v[110:111], v[110:111], 0, s[10:11]
	v_pk_mul_f32 v[34:35], v[34:35], v[38:39]
	v_med3_f32 v38, v40, s81, v170
	v_med3_f32 v39, v41, s81, v170
	v_pk_add_f32 v[40:41], v[54:55], 1.0 op_sel_hi:[1,0]
	v_lshl_add_u64 v[66:67], v[110:111], 0, v[142:143]
	v_rcp_f32_e32 v40, v40
	v_rcp_f32_e32 v41, v41
	s_waitcnt lgkmcnt(0)
	global_store_dwordx4 v[66:67], v[42:45], off
	ds_write_b64 v108, v[102:103]
	ds_write_b64 v108, v[86:87] offset:768
	v_or_b32_e32 v66, 32, v106
	v_mov_b32_e32 v55, v143
	ds_read_b128 v[42:45], v109
	v_ashrrev_i32_e32 v67, 31, v66
	v_cvt_pk_fp8_f32 v55, v34, v35
	v_lshlrev_b64 v[66:67], 10, v[66:67]
	v_lshl_add_u64 v[66:67], s[18:19], 0, v[66:67]
	v_pk_mul_f32 v[34:35], v[36:37], v[40:41]
	v_mul_f32_e32 v40, 0x3d800000, v171
	v_lshl_add_u64 v[66:67], v[66:67], 0, s[10:11]
	v_pk_mul_f32 v[34:35], v[34:35], v[38:39]
	v_pk_fma_f32 v[26:27], v[40:41], v[26:27], v[160:161] op_sel_hi:[0,1,1]
	v_cvt_pk_fp8_f32 v55, v34, v35 op_sel:[0,0,1]
	v_lshl_add_u64 v[34:35], v[66:67], 0, v[142:143]
	v_min_f32_e32 v26, 0x41898193, v26
	v_min_f32_e32 v27, 0x41898193, v27
	s_waitcnt lgkmcnt(0)
	global_store_dwordx4 v[34:35], v[42:45], off
	v_pk_fma_f32 v[28:29], v[40:41], v[28:29], v[154:155] op_sel_hi:[0,1,1]
	v_min_f32_e32 v28, 0x41898193, v28
	v_exp_f32_e64 v42, -v26
	v_exp_f32_e64 v43, -v27
	v_min_f32_e32 v29, 0x41898193, v29
	v_exp_f32_e64 v44, -v28
	v_exp_f32_e64 v45, -v29
	v_pk_add_f32 v[42:43], v[42:43], 1.0 op_sel_hi:[1,0]
	v_pk_fma_f32 v[30:31], v[40:41], v[30:31], v[156:157] op_sel_hi:[0,1,1]
	v_rcp_f32_e32 v42, v42
	v_rcp_f32_e32 v43, v43
	v_pk_fma_f32 v[18:19], v[40:41], v[18:19], v[152:153] op_sel_hi:[0,1,1]
	v_pk_fma_f32 v[32:33], v[40:41], v[32:33], v[158:159] op_sel_hi:[0,1,1]
	v_med3_f32 v30, v30, s81, v170
	v_pk_mul_f32 v[26:27], v[26:27], v[42:43]
	v_pk_add_f32 v[42:43], v[44:45], 1.0 op_sel_hi:[1,0]
	v_med3_f32 v31, v31, s81, v170
	v_rcp_f32_e32 v42, v42
	v_rcp_f32_e32 v43, v43
	v_min_f32_e32 v18, 0x41898193, v18
	v_min_f32_e32 v19, 0x41898193, v19
	v_pk_mul_f32 v[26:27], v[26:27], v[30:31]
	v_med3_f32 v30, v32, s81, v170
	v_med3_f32 v31, v33, s81, v170
	v_exp_f32_e64 v32, -v18
	v_exp_f32_e64 v33, -v19
	v_pk_mul_f32 v[28:29], v[28:29], v[42:43]
	v_pk_fma_f32 v[20:21], v[40:41], v[20:21], v[48:49] op_sel_hi:[0,1,1]
	v_pk_mul_f32 v[28:29], v[28:29], v[30:31]
	v_pk_add_f32 v[30:31], v[32:33], 1.0 op_sel_hi:[1,0]
	v_min_f32_e32 v20, 0x41898193, v20
	v_rcp_f32_e32 v30, v30
	v_rcp_f32_e32 v31, v31
	v_min_f32_e32 v21, 0x41898193, v21
	v_pk_fma_f32 v[22:23], v[40:41], v[22:23], v[46:47] op_sel_hi:[0,1,1]
	v_pk_fma_f32 v[24:25], v[40:41], v[24:25], v[150:151] op_sel_hi:[0,1,1]
	v_pk_mul_f32 v[18:19], v[18:19], v[30:31]
	v_exp_f32_e64 v30, -v20
	v_exp_f32_e64 v31, -v21
	v_med3_f32 v22, v22, s81, v170
	v_med3_f32 v23, v23, s81, v170
	v_pk_mul_f32 v[18:19], v[18:19], v[22:23]
	v_med3_f32 v22, v24, s81, v170
	v_med3_f32 v23, v25, s81, v170
	v_pk_add_f32 v[24:25], v[30:31], 1.0 op_sel_hi:[1,0]
	v_mov_b32_e32 v31, v143
	v_rcp_f32_e32 v24, v24
	v_rcp_f32_e32 v25, v25
	v_cvt_pk_fp8_f32 v31, v18, v19
	v_med3_f32 v78, v78, s81, v170
	v_med3_f32 v79, v79, s81, v170
	v_pk_mul_f32 v[18:19], v[20:21], v[24:25]
	v_pk_mul_f32 v[70:71], v[70:71], v[78:79]
	v_pk_mul_f32 v[18:19], v[18:19], v[22:23]
	v_mov_b32_e32 v68, v143
	v_cvt_pk_fp8_f32 v31, v18, v19 op_sel:[0,0,1]
	v_mul_f32_e32 v18, 0x3d800000, v169
	v_pk_fma_f32 v[10:11], v[18:19], v[10:11], v[160:161] op_sel_hi:[0,1,1]
	v_min_f32_e32 v10, 0x41898193, v10
	v_min_f32_e32 v11, 0x41898193, v11
	v_exp_f32_e64 v20, -v10
	v_exp_f32_e64 v21, -v11
	v_pk_fma_f32 v[12:13], v[18:19], v[12:13], v[154:155] op_sel_hi:[0,1,1]
	v_min_f32_e32 v12, 0x41898193, v12
	v_min_f32_e32 v13, 0x41898193, v13
	v_pk_add_f32 v[20:21], v[20:21], 1.0 op_sel_hi:[1,0]
	v_exp_f32_e64 v22, -v12
	v_rcp_f32_e32 v20, v20
	v_rcp_f32_e32 v21, v21
	v_exp_f32_e64 v23, -v13
	v_pk_fma_f32 v[14:15], v[18:19], v[14:15], v[156:157] op_sel_hi:[0,1,1]
	v_pk_fma_f32 v[2:3], v[18:19], v[2:3], v[152:153] op_sel_hi:[0,1,1]
	v_pk_mul_f32 v[10:11], v[10:11], v[20:21]
	v_pk_add_f32 v[20:21], v[22:23], 1.0 op_sel_hi:[1,0]
	v_pk_fma_f32 v[16:17], v[18:19], v[16:17], v[158:159] op_sel_hi:[0,1,1]
	v_med3_f32 v14, v14, s81, v170
	v_med3_f32 v15, v15, s81, v170
	v_rcp_f32_e32 v20, v20
	v_rcp_f32_e32 v21, v21
	v_min_f32_e32 v2, 0x41898193, v2
	v_min_f32_e32 v3, 0x41898193, v3
	v_pk_mul_f32 v[10:11], v[10:11], v[14:15]
	v_med3_f32 v14, v16, s81, v170
	v_med3_f32 v15, v17, s81, v170
	v_exp_f32_e64 v16, -v2
	v_exp_f32_e64 v17, -v3
	v_pk_mul_f32 v[12:13], v[12:13], v[20:21]
	v_pk_fma_f32 v[4:5], v[18:19], v[4:5], v[48:49] op_sel_hi:[0,1,1]
	v_pk_mul_f32 v[12:13], v[12:13], v[14:15]
	v_pk_add_f32 v[14:15], v[16:17], 1.0 op_sel_hi:[1,0]
	v_min_f32_e32 v4, 0x41898193, v4
	v_rcp_f32_e32 v14, v14
	v_rcp_f32_e32 v15, v15
	v_min_f32_e32 v5, 0x41898193, v5
	v_cvt_pk_fp8_f32 v68, v70, v71
	v_mov_b32_e32 v54, v143
	v_pk_mul_f32 v[2:3], v[2:3], v[14:15]
	v_exp_f32_e64 v14, -v4
	v_exp_f32_e64 v15, -v5
	v_cvt_pk_fp8_f32 v54, v50, v51
	v_med3_f32 v76, v76, s81, v170
	v_med3_f32 v77, v77, s81, v170
	v_pk_fma_f32 v[6:7], v[18:19], v[6:7], v[46:47] op_sel_hi:[0,1,1]
	v_pk_mul_f32 v[72:73], v[72:73], v[76:77]
	v_pk_fma_f32 v[8:9], v[18:19], v[8:9], v[150:151] op_sel_hi:[0,1,1]
	v_med3_f32 v6, v6, s81, v170
	v_med3_f32 v7, v7, s81, v170
	v_cvt_pk_fp8_f32 v68, v72, v73 op_sel:[0,0,1]
	v_pk_mul_f32 v[2:3], v[2:3], v[6:7]
	v_med3_f32 v6, v8, s81, v170
	v_med3_f32 v7, v9, s81, v170
	v_pk_add_f32 v[8:9], v[14:15], 1.0 op_sel_hi:[1,0]
	v_cvt_pk_fp8_f32 v54, v52, v53 op_sel:[0,0,1]
	v_mov_b32_e32 v30, v143
	v_rcp_f32_e32 v8, v8
	v_rcp_f32_e32 v9, v9
	v_cvt_pk_fp8_f32 v30, v26, v27
	v_mov_b32_e32 v14, v143
	v_mov_b32_e32 v15, v143
	v_cvt_pk_fp8_f32 v14, v10, v11
	v_cvt_pk_fp8_f32 v15, v2, v3
	ds_write_b64 v108, v[68:69]
	ds_write_b64 v108, v[54:55] offset:768
	v_add_u32_e32 v38, 0x80, v106
	ds_read_b128 v[34:37], v109
	v_ashrrev_i32_e32 v39, 31, v38
	v_pk_mul_f32 v[2:3], v[4:5], v[8:9]
	v_lshlrev_b64 v[38:39], 10, v[38:39]
	v_cvt_pk_fp8_f32 v30, v28, v29 op_sel:[0,0,1]
	v_pk_mul_f32 v[2:3], v[2:3], v[6:7]
	v_lshl_add_u64 v[38:39], s[18:19], 0, v[38:39]
	v_cvt_pk_fp8_f32 v14, v12, v13 op_sel:[0,0,1]
	v_cvt_pk_fp8_f32 v15, v2, v3 op_sel:[0,0,1]
	v_lshl_add_u64 v[38:39], v[38:39], 0, s[10:11]
	v_lshl_add_u64 v[2:3], v[38:39], 0, v[142:143]
	s_waitcnt lgkmcnt(0)
	global_store_dwordx4 v[2:3], v[34:37], off
	ds_write_b64 v108, v[30:31]
	ds_write_b64 v108, v[14:15] offset:768
	v_add_u32_e32 v6, 0xa0, v106
	ds_read_b128 v[2:5], v109
	v_ashrrev_i32_e32 v7, 31, v6
	v_lshlrev_b64 v[6:7], 10, v[6:7]
	v_lshl_add_u64 v[6:7], s[18:19], 0, v[6:7]
	v_lshl_add_u64 v[6:7], v[6:7], 0, s[10:11]
	v_lshl_add_u64 v[6:7], v[6:7], 0, v[142:143]
	s_and_b64 vcc, exec, s[8:9]
	s_mov_b64 s[8:9], -1
	s_waitcnt lgkmcnt(0)
	global_store_dwordx4 v[6:7], v[2:5], off
	s_cbranch_vccnz .LBB0_3339
	s_lshl_b64 s[8:9], s[70:71], 12
	s_add_u32 s11, s6, s8
	s_addc_u32 s65, s7, s9
	s_lshl_b32 s8, s64, 7
	s_ashr_i32 s9, s8, 31
	v_mov_b32_e32 v2, v0
	s_lshl_b64 s[8:9], s[8:9], 1
	s_add_u32 s8, s11, s8
	v_readfirstlane_b32 s10, v2
	s_addc_u32 s9, s65, s9
	s_and_b32 s11, s10, 0xc0
	s_add_u32 s8, s8, s11
	s_addc_u32 s9, s9, 0
	v_and_b32_e32 v3, 48, v2
	global_load_dwordx4 v[46:49], v3, s[8:9]
	global_load_dwordx4 v[42:45], v3, s[8:9] offset:2048
	s_ashr_i32 s9, s10, 2
	s_lshl_b32 s8, s66, 8
	s_andn2_b32 s9, s9, 63
	s_add_i32 s9, s9, s8
	v_and_or_b32 v2, v2, 15, s9
	v_ashrrev_i32_e32 v3, 31, v2
	v_lshl_add_u64 v[4:5], v[2:3], 2, s[14:15]
	v_add_u32_e32 v6, 0x80, v2
	v_add_u32_e32 v8, 0x90, v2
	v_add_u32_e32 v10, 0xa0, v2
	v_add_u32_e32 v2, 0xb0, v2
	v_ashrrev_i32_e32 v7, 31, v6
	v_ashrrev_i32_e32 v9, 31, v8
	v_ashrrev_i32_e32 v11, 31, v10
	v_ashrrev_i32_e32 v3, 31, v2
	v_lshl_add_u64 v[6:7], v[6:7], 2, s[14:15]
	v_lshl_add_u64 v[8:9], v[8:9], 2, s[14:15]
	v_lshl_add_u64 v[10:11], v[10:11], 2, s[14:15]
	v_lshl_add_u64 v[2:3], v[2:3], 2, s[14:15]
	global_load_dword v179, v[4:5], off
	global_load_dword v178, v[4:5], off offset:64
	global_load_dword v177, v[4:5], off offset:128
	global_load_dword v176, v[4:5], off offset:192
	global_load_dword v175, v[6:7], off
	global_load_dword v174, v[8:9], off
	global_load_dword v171, v[10:11], off
	global_load_dword v169, v[2:3], off
	s_andn2_b64 vcc, exec, s[16:17]
	s_cbranch_vccnz .LBB0_3338
	s_barrier
	s_branch .LBB0_3338

.LBB0_3429:
	v_lshlrev_b32_e32 v158, 16, v6
	v_and_b32_e32 v159, 0xffff0000, v6
	v_lshlrev_b32_e32 v154, 16, v8
	v_and_b32_e32 v155, 0xffff0000, v8
	v_lshlrev_b32_e32 v156, 16, v7
	v_and_b32_e32 v157, 0xffff0000, v7
	v_lshlrev_b32_e32 v152, 16, v9
	v_and_b32_e32 v153, 0xffff0000, v9
	s_waitcnt vmcnt(10)
	v_lshlrev_b32_e32 v6, 16, v4
	v_and_b32_e32 v7, 0xffff0000, v4
	v_mul_f32_e32 v4, 0x41000000, v146
	v_pk_fma_f32 v[134:135], v[134:135], s[38:39], v[158:159] op_sel_hi:[1,0,1]
	v_pk_fma_f32 v[130:131], v[130:131], s[38:39], v[154:155] op_sel_hi:[1,0,1]
	v_pk_fma_f32 v[136:137], v[136:137], s[38:39], v[156:157] op_sel_hi:[1,0,1]
	v_pk_mul_f32 v[134:135], v[4:5], v[134:135] op_sel_hi:[0,1]
	v_pk_fma_f32 v[132:133], v[132:133], s[38:39], v[152:153] op_sel_hi:[1,0,1]
	v_pk_mul_f32 v[130:131], v[4:5], v[130:131] op_sel_hi:[0,1]
	v_lshlrev_b32_e32 v150, 16, v2
	v_and_b32_e32 v151, 0xffff0000, v2
	v_lshlrev_b32_e32 v8, 16, v3
	v_and_b32_e32 v9, 0xffff0000, v3
	v_lshlrev_b32_e32 v2, 16, v5
	v_and_b32_e32 v3, 0xffff0000, v5
	v_pk_mul_f32 v[136:137], v[4:5], v[136:137] op_sel_hi:[0,1]
	v_pk_mul_f32 v[132:133], v[4:5], v[132:133] op_sel_hi:[0,1]
	v_med3_f32 v5, v134, s75, v164
	v_med3_f32 v134, v130, s75, v164
	v_med3_f32 v135, v135, s75, v164
	v_mov_b32_e32 v130, 0
	v_cvt_pk_fp8_f32 v130, v5, v135
	v_med3_f32 v136, v136, s75, v164
	v_med3_f32 v5, v137, s75, v164
	v_pk_fma_f32 v[126:127], v[126:127], s[38:39], v[150:151] op_sel_hi:[1,0,1]
	v_pk_fma_f32 v[128:129], v[128:129], s[38:39], v[8:9] op_sel_hi:[1,0,1]
	v_pk_fma_f32 v[122:123], v[122:123], s[38:39], v[6:7] op_sel_hi:[1,0,1]
	v_pk_fma_f32 v[124:125], v[124:125], s[38:39], v[2:3] op_sel_hi:[1,0,1]
	v_cvt_pk_fp8_f32 v130, v136, v5 op_sel:[0,0,1]
	v_pk_mul_f32 v[128:129], v[4:5], v[128:129] op_sel_hi:[0,1]
	v_pk_mul_f32 v[126:127], v[4:5], v[126:127] op_sel_hi:[0,1]
	v_pk_mul_f32 v[124:125], v[4:5], v[124:125] op_sel_hi:[0,1]
	v_pk_mul_f32 v[4:5], v[4:5], v[122:123] op_sel_hi:[0,1]
	v_med3_f32 v146, v131, s75, v164
	v_mov_b32_e32 v131, 0
	v_med3_f32 v122, v126, s75, v164
	v_med3_f32 v123, v4, s75, v164
	v_med3_f32 v126, v127, s75, v164
	v_med3_f32 v127, v5, s75, v164
	v_mov_b32_e32 v4, 0
	v_mov_b32_e32 v5, 0
	v_cvt_pk_fp8_f32 v131, v134, v146
	v_cvt_pk_fp8_f32 v4, v122, v126
	v_cvt_pk_fp8_f32 v5, v123, v127
	v_mov_b32_e32 v171, v0
	v_med3_f32 v132, v132, s75, v164
	v_readfirstlane_b32 s41, v171
	s_lshr_b32 s8, s41, 6
	v_med3_f32 v133, v133, s75, v164
	v_med3_f32 v128, v128, s75, v164
	v_med3_f32 v124, v124, s75, v164
	v_med3_f32 v122, v129, s75, v164
	v_med3_f32 v123, v125, s75, v164
	s_mulk_i32 s8, 0xb00
	v_cvt_pk_fp8_f32 v131, v132, v133 op_sel:[0,0,1]
	v_cvt_pk_fp8_f32 v4, v128, v122 op_sel:[0,0,1]
	v_cvt_pk_fp8_f32 v5, v124, v123 op_sel:[0,0,1]
	s_add_i32 s8, s8, 0
	v_and_b32_e32 v172, 15, v171
	v_lshrrev_b32_e32 v123, 1, v171
	s_add_i32 s43, s8, 0x20000
	v_mul_u32_u24_e32 v122, 0x50, v172
	v_and_b32_e32 v123, 24, v123
	v_add3_u32 v122, s43, v122, v123
	s_and_b32 s9, s41, 0xc0
	ds_write2_b64 v122, v[130:131], v[4:5] offset1:4
	v_bfe_u32 v4, v171, 2, 4
	s_ashr_i32 s41, s41, 2
	v_mul_u32_u24_e32 v5, 0x50, v4
	v_lshlrev_b32_e32 v123, 4, v171
	s_andn2_b32 s41, s41, 63
	v_lshl_or_b32 v4, s50, 8, v4
	v_and_b32_e32 v146, 48, v123
	v_add_u32_e32 v4, s41, v4
	v_mul_f32_e32 v130, 0x41000000, v170
	v_pk_fma_f32 v[118:119], v[118:119], s[38:39], v[158:159] op_sel_hi:[1,0,1]
	v_pk_fma_f32 v[114:115], v[114:115], s[38:39], v[154:155] op_sel_hi:[1,0,1]
	v_add3_u32 v123, s43, v5, v146
	v_ashrrev_i32_e32 v5, 31, v4
	v_pk_mul_f32 v[118:119], v[130:131], v[118:119] op_sel_hi:[0,1]
	v_pk_mul_f32 v[114:115], v[130:131], v[114:115] op_sel_hi:[0,1]
	v_lshlrev_b64 v[128:129], 10, v[4:5]
	v_med3_f32 v5, v118, s75, v164
	v_med3_f32 v118, v114, s75, v164
	v_med3_f32 v119, v119, s75, v164
	v_mov_b32_e32 v114, v147
	v_cvt_pk_fp8_f32 v114, v5, v119
	v_pk_fma_f32 v[120:121], v[120:121], s[38:39], v[156:157] op_sel_hi:[1,0,1]
	v_pk_fma_f32 v[116:117], v[116:117], s[38:39], v[152:153] op_sel_hi:[1,0,1]
	v_pk_mul_f32 v[120:121], v[130:131], v[120:121] op_sel_hi:[0,1]
	v_pk_mul_f32 v[116:117], v[130:131], v[116:117] op_sel_hi:[0,1]
	v_med3_f32 v131, v115, s75, v164
	v_pk_fma_f32 v[110:111], v[110:111], s[38:39], v[150:151] op_sel_hi:[1,0,1]
	v_pk_fma_f32 v[106:107], v[106:107], s[38:39], v[6:7] op_sel_hi:[1,0,1]
	v_med3_f32 v120, v120, s75, v164
	v_med3_f32 v5, v121, s75, v164
	v_pk_mul_f32 v[110:111], v[130:131], v[110:111] op_sel_hi:[0,1]
	v_pk_mul_f32 v[106:107], v[130:131], v[106:107] op_sel_hi:[0,1]
	v_cvt_pk_fp8_f32 v114, v120, v5 op_sel:[0,0,1]
	v_med3_f32 v5, v110, s75, v164
	v_med3_f32 v110, v106, s75, v164
	v_med3_f32 v111, v111, s75, v164
	v_mov_b32_e32 v106, v147
	v_cvt_pk_fp8_f32 v106, v5, v111
	v_pk_fma_f32 v[112:113], v[112:113], s[38:39], v[8:9] op_sel_hi:[1,0,1]
	v_mov_b32_e32 v115, v147
	v_pk_mul_f32 v[112:113], v[130:131], v[112:113] op_sel_hi:[0,1]
	v_med3_f32 v112, v112, s75, v164
	v_med3_f32 v5, v113, s75, v164
	v_cvt_pk_fp8_f32 v106, v112, v5 op_sel:[0,0,1]
	v_mul_f32_e32 v112, 0x41000000, v169
	v_pk_fma_f32 v[102:103], v[102:103], s[38:39], v[158:159] op_sel_hi:[1,0,1]
	v_pk_fma_f32 v[98:99], v[98:99], s[38:39], v[154:155] op_sel_hi:[1,0,1]
	v_cvt_pk_fp8_f32 v115, v118, v131
	v_pk_mul_f32 v[102:103], v[112:113], v[102:103] op_sel_hi:[0,1]
	v_pk_mul_f32 v[98:99], v[112:113], v[98:99] op_sel_hi:[0,1]
	v_med3_f32 v5, v102, s75, v164
	v_med3_f32 v102, v98, s75, v164
	v_med3_f32 v103, v103, s75, v164
	v_mov_b32_e32 v98, v147
	v_cvt_pk_fp8_f32 v98, v5, v103
	v_med3_f32 v116, v116, s75, v164
	v_med3_f32 v117, v117, s75, v164
	v_pk_fma_f32 v[104:105], v[104:105], s[38:39], v[156:157] op_sel_hi:[1,0,1]
	v_pk_fma_f32 v[100:101], v[100:101], s[38:39], v[152:153] op_sel_hi:[1,0,1]
	v_cvt_pk_fp8_f32 v115, v116, v117 op_sel:[0,0,1]
	v_med3_f32 v116, v107, s75, v164
	v_mov_b32_e32 v107, v147
	v_pk_mul_f32 v[104:105], v[112:113], v[104:105] op_sel_hi:[0,1]
	v_pk_mul_f32 v[100:101], v[112:113], v[100:101] op_sel_hi:[0,1]
	v_med3_f32 v113, v99, s75, v164
	v_pk_fma_f32 v[94:95], v[94:95], s[38:39], v[150:151] op_sel_hi:[1,0,1]
	v_pk_fma_f32 v[90:91], v[90:91], s[38:39], v[6:7] op_sel_hi:[1,0,1]
	v_cvt_pk_fp8_f32 v107, v110, v116
	v_med3_f32 v104, v104, s75, v164
	v_med3_f32 v5, v105, s75, v164
	v_pk_mul_f32 v[94:95], v[112:113], v[94:95] op_sel_hi:[0,1]
	v_pk_mul_f32 v[90:91], v[112:113], v[90:91] op_sel_hi:[0,1]
	v_pk_fma_f32 v[108:109], v[108:109], s[38:39], v[2:3] op_sel_hi:[1,0,1]
	v_mov_b32_e32 v99, v147
	v_cvt_pk_fp8_f32 v98, v104, v5 op_sel:[0,0,1]
	v_med3_f32 v5, v94, s75, v164
	v_med3_f32 v94, v90, s75, v164
	v_med3_f32 v95, v95, s75, v164
	v_mov_b32_e32 v90, v147
	s_lshl_b32 s8, s62, 8
	ds_read_b128 v[124:127], v123
	v_pk_mul_f32 v[108:109], v[130:131], v[108:109] op_sel_hi:[0,1]
	v_cvt_pk_fp8_f32 v99, v102, v113
	v_cvt_pk_fp8_f32 v90, v5, v95
	s_or_b32 s8, s9, s8
	v_med3_f32 v108, v108, s75, v164
	v_med3_f32 v109, v109, s75, v164
	v_pk_fma_f32 v[96:97], v[96:97], s[38:39], v[8:9] op_sel_hi:[1,0,1]
	s_ashr_i32 s9, s8, 31
	v_lshl_add_u64 v[128:129], s[16:17], 0, v[128:129]
	v_cvt_pk_fp8_f32 v107, v108, v109 op_sel:[0,0,1]
	v_pk_mul_f32 v[96:97], v[112:113], v[96:97] op_sel_hi:[0,1]
	v_lshl_add_u64 v[128:129], v[128:129], 0, s[8:9]
	v_med3_f32 v100, v100, s75, v164
	v_med3_f32 v101, v101, s75, v164
	v_med3_f32 v96, v96, s75, v164
	v_med3_f32 v5, v97, s75, v164
	v_lshl_add_u64 v[108:109], v[128:129], 0, v[146:147]
	v_cvt_pk_fp8_f32 v99, v100, v101 op_sel:[0,0,1]
	v_med3_f32 v100, v91, s75, v164
	v_mov_b32_e32 v91, v147
	v_cvt_pk_fp8_f32 v90, v96, v5 op_sel:[0,0,1]
	v_mul_f32_e32 v96, 0x41000000, v168
	v_pk_fma_f32 v[78:79], v[78:79], s[38:39], v[158:159] op_sel_hi:[1,0,1]
	v_pk_fma_f32 v[74:75], v[74:75], s[38:39], v[154:155] op_sel_hi:[1,0,1]
	s_waitcnt lgkmcnt(0)
	global_store_dwordx4 v[108:109], v[124:127], off
	v_cvt_pk_fp8_f32 v91, v94, v100
	v_pk_fma_f32 v[80:81], v[80:81], s[38:39], v[156:157] op_sel_hi:[1,0,1]
	v_pk_mul_f32 v[78:79], v[96:97], v[78:79] op_sel_hi:[0,1]
	v_pk_fma_f32 v[76:77], v[76:77], s[38:39], v[152:153] op_sel_hi:[1,0,1]
	v_pk_mul_f32 v[74:75], v[96:97], v[74:75] op_sel_hi:[0,1]
	ds_write2_b64 v122, v[114:115], v[106:107] offset1:4
	v_or_b32_e32 v110, 16, v4
	v_pk_fma_f32 v[92:93], v[92:93], s[38:39], v[2:3] op_sel_hi:[1,0,1]
	v_pk_mul_f32 v[80:81], v[96:97], v[80:81] op_sel_hi:[0,1]
	v_pk_mul_f32 v[76:77], v[96:97], v[76:77] op_sel_hi:[0,1]
	v_med3_f32 v5, v78, s75, v164
	v_med3_f32 v78, v74, s75, v164
	v_med3_f32 v79, v79, s75, v164
	v_med3_f32 v97, v75, s75, v164
	v_mov_b32_e32 v74, v147
	v_mov_b32_e32 v75, v147
	ds_read_b128 v[106:109], v123
	v_ashrrev_i32_e32 v111, 31, v110
	v_pk_mul_f32 v[92:93], v[112:113], v[92:93] op_sel_hi:[0,1]
	v_cvt_pk_fp8_f32 v74, v5, v79
	v_cvt_pk_fp8_f32 v75, v78, v97
	v_lshlrev_b64 v[110:111], 10, v[110:111]
	v_med3_f32 v92, v92, s75, v164
	v_med3_f32 v93, v93, s75, v164
	v_lshl_add_u64 v[110:111], s[16:17], 0, v[110:111]
	v_cvt_pk_fp8_f32 v91, v92, v93 op_sel:[0,0,1]
	v_pk_fma_f32 v[62:63], v[62:63], s[38:39], v[150:151] op_sel_hi:[1,0,1]
	v_pk_fma_f32 v[58:59], v[58:59], s[38:39], v[6:7] op_sel_hi:[1,0,1]
	v_lshl_add_u64 v[110:111], v[110:111], 0, s[8:9]
	v_med3_f32 v80, v80, s75, v164
	v_med3_f32 v76, v76, s75, v164
	v_med3_f32 v5, v81, s75, v164
	v_med3_f32 v77, v77, s75, v164
	v_pk_mul_f32 v[62:63], v[96:97], v[62:63] op_sel_hi:[0,1]
	v_pk_mul_f32 v[58:59], v[96:97], v[58:59] op_sel_hi:[0,1]
	v_lshl_add_u64 v[92:93], v[110:111], 0, v[146:147]
	v_cvt_pk_fp8_f32 v74, v80, v5 op_sel:[0,0,1]
	v_cvt_pk_fp8_f32 v75, v76, v77 op_sel:[0,0,1]
	v_med3_f32 v5, v62, s75, v164
	v_med3_f32 v62, v58, s75, v164
	v_med3_f32 v63, v63, s75, v164
	v_med3_f32 v76, v59, s75, v164
	v_mov_b32_e32 v58, v147
	v_mov_b32_e32 v59, v147
	s_waitcnt lgkmcnt(0)
	global_store_dwordx4 v[92:93], v[106:109], off
	s_cmp_lg_u64 s[20:21], 0
	s_cbranch_scc0 .Lepibar_dn1
	s_barrier
.Lepibar_dn1:
	v_cvt_pk_fp8_f32 v58, v5, v63
	v_cvt_pk_fp8_f32 v59, v62, v76
	ds_write2_b64 v122, v[98:99], v[90:91] offset1:4
	v_or_b32_e32 v94, 32, v4
	v_pk_fma_f32 v[64:65], v[64:65], s[38:39], v[8:9] op_sel_hi:[1,0,1]
	v_pk_fma_f32 v[60:61], v[60:61], s[38:39], v[2:3] op_sel_hi:[1,0,1]
	ds_read_b128 v[90:93], v123
	v_ashrrev_i32_e32 v95, 31, v94
	v_pk_mul_f32 v[64:65], v[96:97], v[64:65] op_sel_hi:[0,1]
	v_pk_mul_f32 v[60:61], v[96:97], v[60:61] op_sel_hi:[0,1]
	v_lshlrev_b64 v[94:95], 10, v[94:95]
	v_med3_f32 v64, v64, s75, v164
	v_med3_f32 v60, v60, s75, v164
	v_med3_f32 v5, v65, s75, v164
	v_med3_f32 v61, v61, s75, v164
	v_lshl_add_u64 v[94:95], s[16:17], 0, v[94:95]
	v_cvt_pk_fp8_f32 v58, v64, v5 op_sel:[0,0,1]
	v_cvt_pk_fp8_f32 v59, v60, v61 op_sel:[0,0,1]
	v_lshl_add_u64 v[94:95], v[94:95], 0, s[8:9]
	v_lshl_add_u64 v[60:61], v[94:95], 0, v[146:147]
	s_waitcnt lgkmcnt(0)
	global_store_dwordx4 v[60:61], v[90:93], off
	ds_write2_b64 v122, v[74:75], v[58:59] offset1:4
	v_mul_f32_e32 v64, 0x41000000, v167
	v_pk_fma_f32 v[74:75], v[86:87], s[38:39], v[158:159] op_sel_hi:[1,0,1]
	v_pk_fma_f32 v[78:79], v[82:83], s[38:39], v[154:155] op_sel_hi:[1,0,1]
	v_pk_mul_f32 v[74:75], v[64:65], v[74:75] op_sel_hi:[0,1]
	v_pk_fma_f32 v[76:77], v[88:89], s[38:39], v[156:157] op_sel_hi:[1,0,1]
	v_pk_fma_f32 v[80:81], v[84:85], s[38:39], v[152:153] op_sel_hi:[1,0,1]
	v_pk_mul_f32 v[78:79], v[64:65], v[78:79] op_sel_hi:[0,1]
	v_med3_f32 v5, v74, s75, v164
	v_med3_f32 v75, v75, s75, v164
	v_mov_b32_e32 v74, v147
	v_pk_mul_f32 v[76:77], v[64:65], v[76:77] op_sel_hi:[0,1]
	v_pk_mul_f32 v[80:81], v[64:65], v[80:81] op_sel_hi:[0,1]
	v_med3_f32 v65, v78, s75, v164
	v_med3_f32 v78, v79, s75, v164
	v_cvt_pk_fp8_f32 v74, v5, v75
	v_mov_b32_e32 v75, v147
	v_cvt_pk_fp8_f32 v75, v65, v78
	v_med3_f32 v79, v80, s75, v164
	v_med3_f32 v65, v81, s75, v164
	v_pk_fma_f32 v[70:71], v[70:71], s[38:39], v[150:151] op_sel_hi:[1,0,1]
	v_pk_fma_f32 v[72:73], v[72:73], s[38:39], v[8:9] op_sel_hi:[1,0,1]
	v_pk_fma_f32 v[66:67], v[66:67], s[38:39], v[6:7] op_sel_hi:[1,0,1]
	v_pk_fma_f32 v[68:69], v[68:69], s[38:39], v[2:3] op_sel_hi:[1,0,1]
	v_med3_f32 v76, v76, s75, v164
	v_med3_f32 v5, v77, s75, v164
	v_cvt_pk_fp8_f32 v75, v79, v65 op_sel:[0,0,1]
	v_pk_mul_f32 v[72:73], v[64:65], v[72:73] op_sel_hi:[0,1]
	v_pk_mul_f32 v[70:71], v[64:65], v[70:71] op_sel_hi:[0,1]
	v_pk_mul_f32 v[68:69], v[64:65], v[68:69] op_sel_hi:[0,1]
	v_pk_mul_f32 v[64:65], v[64:65], v[66:67] op_sel_hi:[0,1]
	v_cvt_pk_fp8_f32 v74, v76, v5 op_sel:[0,0,1]
	v_med3_f32 v5, v70, s75, v164
	v_med3_f32 v66, v64, s75, v164
	v_med3_f32 v67, v71, s75, v164
	v_med3_f32 v70, v65, s75, v164
	v_mov_b32_e32 v64, v147
	v_mov_b32_e32 v65, v147
	v_cvt_pk_fp8_f32 v64, v5, v67
	v_cvt_pk_fp8_f32 v65, v66, v70
	v_or_b32_e32 v62, 48, v4
	ds_read_b128 v[58:61], v123
	v_ashrrev_i32_e32 v63, 31, v62
	v_lshlrev_b64 v[62:63], 10, v[62:63]
	v_med3_f32 v71, v72, s75, v164
	v_med3_f32 v68, v68, s75, v164
	v_med3_f32 v5, v73, s75, v164
	v_med3_f32 v66, v69, s75, v164
	v_lshl_add_u64 v[62:63], s[16:17], 0, v[62:63]
	v_cvt_pk_fp8_f32 v64, v71, v5 op_sel:[0,0,1]
	v_cvt_pk_fp8_f32 v65, v68, v66 op_sel:[0,0,1]
	v_lshl_add_u64 v[62:63], v[62:63], 0, s[8:9]
	v_lshl_add_u64 v[62:63], v[62:63], 0, v[146:147]
	s_waitcnt lgkmcnt(0)
	global_store_dwordx4 v[62:63], v[58:61], off
	ds_write2_b64 v122, v[74:75], v[64:65] offset1:4
	v_mul_f32_e32 v64, 0x41000000, v166
	v_pk_fma_f32 v[54:55], v[54:55], s[38:39], v[158:159] op_sel_hi:[1,0,1]
	v_pk_fma_f32 v[50:51], v[50:51], s[38:39], v[154:155] op_sel_hi:[1,0,1]
	v_pk_mul_f32 v[54:55], v[64:65], v[54:55] op_sel_hi:[0,1]
	v_pk_mul_f32 v[50:51], v[64:65], v[50:51] op_sel_hi:[0,1]
	v_med3_f32 v5, v54, s75, v164
	v_med3_f32 v54, v50, s75, v164
	v_med3_f32 v55, v55, s75, v164
	v_mov_b32_e32 v50, v147
	v_cvt_pk_fp8_f32 v50, v5, v55
	v_pk_fma_f32 v[56:57], v[56:57], s[38:39], v[156:157] op_sel_hi:[1,0,1]
	v_pk_fma_f32 v[52:53], v[52:53], s[38:39], v[152:153] op_sel_hi:[1,0,1]
	v_pk_mul_f32 v[56:57], v[64:65], v[56:57] op_sel_hi:[0,1]
	v_pk_mul_f32 v[52:53], v[64:65], v[52:53] op_sel_hi:[0,1]
	v_med3_f32 v65, v51, s75, v164
	v_pk_fma_f32 v[46:47], v[46:47], s[38:39], v[150:151] op_sel_hi:[1,0,1]
	v_pk_fma_f32 v[42:43], v[42:43], s[38:39], v[6:7] op_sel_hi:[1,0,1]
	v_med3_f32 v56, v56, s75, v164
	v_med3_f32 v5, v57, s75, v164
	v_pk_mul_f32 v[46:47], v[64:65], v[46:47] op_sel_hi:[0,1]
	v_pk_mul_f32 v[42:43], v[64:65], v[42:43] op_sel_hi:[0,1]
	v_cvt_pk_fp8_f32 v50, v56, v5 op_sel:[0,0,1]
	v_med3_f32 v5, v46, s75, v164
	v_med3_f32 v46, v42, s75, v164
	v_med3_f32 v47, v47, s75, v164
	v_mov_b32_e32 v42, v147
	v_cvt_pk_fp8_f32 v42, v5, v47
	v_pk_fma_f32 v[48:49], v[48:49], s[38:39], v[8:9] op_sel_hi:[1,0,1]
	v_mov_b32_e32 v51, v147
	v_pk_mul_f32 v[48:49], v[64:65], v[48:49] op_sel_hi:[0,1]
	v_med3_f32 v48, v48, s75, v164
	v_med3_f32 v5, v49, s75, v164
	v_cvt_pk_fp8_f32 v42, v48, v5 op_sel:[0,0,1]
	v_mul_f32_e32 v48, 0x41000000, v165
	v_pk_fma_f32 v[38:39], v[38:39], s[38:39], v[158:159] op_sel_hi:[1,0,1]
	v_pk_fma_f32 v[34:35], v[34:35], s[38:39], v[154:155] op_sel_hi:[1,0,1]
	v_cvt_pk_fp8_f32 v51, v54, v65
	v_pk_mul_f32 v[38:39], v[48:49], v[38:39] op_sel_hi:[0,1]
	v_pk_mul_f32 v[34:35], v[48:49], v[34:35] op_sel_hi:[0,1]
	v_med3_f32 v5, v38, s75, v164
	v_med3_f32 v38, v34, s75, v164
	v_med3_f32 v39, v39, s75, v164
	v_mov_b32_e32 v34, v147
	v_cvt_pk_fp8_f32 v34, v5, v39
	v_med3_f32 v52, v52, s75, v164
	v_med3_f32 v53, v53, s75, v164
	v_pk_fma_f32 v[40:41], v[40:41], s[38:39], v[156:157] op_sel_hi:[1,0,1]
	v_pk_fma_f32 v[36:37], v[36:37], s[38:39], v[152:153] op_sel_hi:[1,0,1]
	v_cvt_pk_fp8_f32 v51, v52, v53 op_sel:[0,0,1]
	v_med3_f32 v52, v43, s75, v164
	v_mov_b32_e32 v43, v147
	v_pk_mul_f32 v[40:41], v[48:49], v[40:41] op_sel_hi:[0,1]
	v_pk_mul_f32 v[36:37], v[48:49], v[36:37] op_sel_hi:[0,1]
	v_med3_f32 v49, v35, s75, v164
	v_pk_fma_f32 v[30:31], v[30:31], s[38:39], v[150:151] op_sel_hi:[1,0,1]
	v_pk_fma_f32 v[26:27], v[26:27], s[38:39], v[6:7] op_sel_hi:[1,0,1]
	v_cvt_pk_fp8_f32 v43, v46, v52
	v_med3_f32 v40, v40, s75, v164
	v_med3_f32 v5, v41, s75, v164
	v_pk_mul_f32 v[30:31], v[48:49], v[30:31] op_sel_hi:[0,1]
	v_pk_mul_f32 v[26:27], v[48:49], v[26:27] op_sel_hi:[0,1]
	v_add_u32_e32 v62, 0x80, v4
	v_pk_fma_f32 v[44:45], v[44:45], s[38:39], v[2:3] op_sel_hi:[1,0,1]
	v_mov_b32_e32 v35, v147
	v_cvt_pk_fp8_f32 v34, v40, v5 op_sel:[0,0,1]
	v_med3_f32 v5, v30, s75, v164
	v_med3_f32 v30, v26, s75, v164
	v_med3_f32 v31, v31, s75, v164
	v_mov_b32_e32 v26, v147
	ds_read_b128 v[58:61], v123
	v_ashrrev_i32_e32 v63, 31, v62
	v_pk_mul_f32 v[44:45], v[64:65], v[44:45] op_sel_hi:[0,1]
	v_cvt_pk_fp8_f32 v35, v38, v49
	v_cvt_pk_fp8_f32 v26, v5, v31
	v_lshlrev_b64 v[62:63], 10, v[62:63]
	v_med3_f32 v44, v44, s75, v164
	v_med3_f32 v45, v45, s75, v164
	v_pk_fma_f32 v[32:33], v[32:33], s[38:39], v[8:9] op_sel_hi:[1,0,1]
	v_lshl_add_u64 v[62:63], s[16:17], 0, v[62:63]
	v_cvt_pk_fp8_f32 v43, v44, v45 op_sel:[0,0,1]
	v_pk_mul_f32 v[32:33], v[48:49], v[32:33] op_sel_hi:[0,1]
	v_lshl_add_u64 v[62:63], v[62:63], 0, s[8:9]
	v_med3_f32 v36, v36, s75, v164
	v_med3_f32 v37, v37, s75, v164
	v_med3_f32 v32, v32, s75, v164
	v_med3_f32 v5, v33, s75, v164
	v_lshl_add_u64 v[44:45], v[62:63], 0, v[146:147]
	v_cvt_pk_fp8_f32 v35, v36, v37 op_sel:[0,0,1]
	v_med3_f32 v36, v27, s75, v164
	v_mov_b32_e32 v27, v147
	v_cvt_pk_fp8_f32 v26, v32, v5 op_sel:[0,0,1]
	v_mul_f32_e32 v32, 0x41000000, v1
	v_pk_fma_f32 v[22:23], v[22:23], s[38:39], v[158:159] op_sel_hi:[1,0,1]
	v_pk_fma_f32 v[18:19], v[18:19], s[38:39], v[154:155] op_sel_hi:[1,0,1]
	s_waitcnt lgkmcnt(0)
	global_store_dwordx4 v[44:45], v[58:61], off
	v_cvt_pk_fp8_f32 v27, v30, v36
	v_pk_mul_f32 v[22:23], v[32:33], v[22:23] op_sel_hi:[0,1]
	v_pk_mul_f32 v[18:19], v[32:33], v[18:19] op_sel_hi:[0,1]
	ds_write2_b64 v122, v[50:51], v[42:43] offset1:4
	v_add_u32_e32 v46, 0x90, v4
	v_pk_fma_f32 v[28:29], v[28:29], s[38:39], v[2:3] op_sel_hi:[1,0,1]
	v_med3_f32 v1, v22, s75, v164
	v_med3_f32 v5, v18, s75, v164
	v_med3_f32 v22, v23, s75, v164
	v_med3_f32 v23, v19, s75, v164
	v_mov_b32_e32 v18, v147
	v_mov_b32_e32 v19, v147
	ds_read_b128 v[42:45], v123
	v_ashrrev_i32_e32 v47, 31, v46
	v_pk_mul_f32 v[28:29], v[48:49], v[28:29] op_sel_hi:[0,1]
	v_cvt_pk_fp8_f32 v18, v1, v22
	v_cvt_pk_fp8_f32 v19, v5, v23
	v_lshlrev_b64 v[46:47], 10, v[46:47]
	v_med3_f32 v28, v28, s75, v164
	v_med3_f32 v29, v29, s75, v164
	v_pk_fma_f32 v[24:25], v[24:25], s[38:39], v[156:157] op_sel_hi:[1,0,1]
	v_pk_fma_f32 v[20:21], v[20:21], s[38:39], v[152:153] op_sel_hi:[1,0,1]
	v_lshl_add_u64 v[46:47], s[16:17], 0, v[46:47]
	v_cvt_pk_fp8_f32 v27, v28, v29 op_sel:[0,0,1]
	v_pk_mul_f32 v[24:25], v[32:33], v[24:25] op_sel_hi:[0,1]
	v_pk_mul_f32 v[20:21], v[32:33], v[20:21] op_sel_hi:[0,1]
	v_pk_fma_f32 v[14:15], v[14:15], s[38:39], v[150:151] op_sel_hi:[1,0,1]
	v_pk_fma_f32 v[6:7], v[10:11], s[38:39], v[6:7] op_sel_hi:[1,0,1]
	v_lshl_add_u64 v[46:47], v[46:47], 0, s[8:9]
	v_med3_f32 v24, v24, s75, v164
	v_med3_f32 v20, v20, s75, v164
	v_med3_f32 v1, v25, s75, v164
	v_med3_f32 v5, v21, s75, v164
	v_pk_mul_f32 v[14:15], v[32:33], v[14:15] op_sel_hi:[0,1]
	v_pk_mul_f32 v[6:7], v[32:33], v[6:7] op_sel_hi:[0,1]
	v_lshl_add_u64 v[28:29], v[46:47], 0, v[146:147]
	v_cvt_pk_fp8_f32 v18, v24, v1 op_sel:[0,0,1]
	v_cvt_pk_fp8_f32 v19, v20, v5 op_sel:[0,0,1]
	v_med3_f32 v1, v14, s75, v164
	v_med3_f32 v5, v6, s75, v164
	v_med3_f32 v10, v15, s75, v164
	v_med3_f32 v11, v7, s75, v164
	v_mov_b32_e32 v6, v147
	v_mov_b32_e32 v7, v147
	s_waitcnt lgkmcnt(0)
	global_store_dwordx4 v[28:29], v[42:45], off
	v_cvt_pk_fp8_f32 v6, v1, v10
	v_cvt_pk_fp8_f32 v7, v5, v11
	ds_write2_b64 v122, v[34:35], v[26:27] offset1:4
	v_add_u32_e32 v30, 0xa0, v4
	v_pk_fma_f32 v[8:9], v[16:17], s[38:39], v[8:9] op_sel_hi:[1,0,1]
	v_pk_fma_f32 v[2:3], v[12:13], s[38:39], v[2:3] op_sel_hi:[1,0,1]
	ds_read_b128 v[26:29], v123
	v_ashrrev_i32_e32 v31, 31, v30
	v_pk_mul_f32 v[8:9], v[32:33], v[8:9] op_sel_hi:[0,1]
	v_pk_mul_f32 v[2:3], v[32:33], v[2:3] op_sel_hi:[0,1]
	v_lshlrev_b64 v[30:31], 10, v[30:31]
	v_med3_f32 v8, v8, s75, v164
	v_med3_f32 v2, v2, s75, v164
	v_med3_f32 v1, v9, s75, v164
	v_med3_f32 v3, v3, s75, v164
	v_lshl_add_u64 v[30:31], s[16:17], 0, v[30:31]
	v_cvt_pk_fp8_f32 v6, v8, v1 op_sel:[0,0,1]
	v_cvt_pk_fp8_f32 v7, v2, v3 op_sel:[0,0,1]
	v_lshl_add_u64 v[30:31], v[30:31], 0, s[8:9]
	v_lshl_add_u64 v[2:3], v[30:31], 0, v[146:147]
	s_waitcnt lgkmcnt(0)
	global_store_dwordx4 v[2:3], v[26:29], off
	ds_write2_b64 v122, v[18:19], v[6:7] offset1:4
	v_add_u32_e32 v2, 0xb0, v4
	ds_read_b128 v[6:9], v123
	v_ashrrev_i32_e32 v3, 31, v2
	v_lshlrev_b64 v[2:3], 10, v[2:3]
	v_lshl_add_u64 v[2:3], s[16:17], 0, v[2:3]
	v_lshl_add_u64 v[2:3], v[2:3], 0, s[8:9]
	v_lshl_add_u64 v[2:3], v[2:3], 0, v[146:147]
	s_waitcnt lgkmcnt(0)
	global_store_dwordx4 v[2:3], v[6:9], off
	s_and_b64 vcc, exec, s[10:11]
	s_mov_b64 s[8:9], -1
	s_cbranch_vccnz .LBB0_3418
	v_mov_b32_e32 v12, v0
	s_lshl_b32 s9, s42, 8
	v_readfirstlane_b32 s8, v12
	s_and_b32 s10, s8, 0xc0
	s_ashr_i32 s8, s8, 2
	s_andn2_b32 s8, s8, 63
	s_add_i32 s8, s8, s9
	v_and_or_b32 v2, v12, 15, s8
	v_ashrrev_i32_e32 v3, 31, v2
	s_lshl_b64 s[8:9], s[44:45], 11
	v_lshl_add_u64 v[4:5], v[2:3], 2, s[12:13]
	v_add_u32_e32 v6, 0x80, v2
	v_add_u32_e32 v8, 0x90, v2
	v_add_u32_e32 v10, 0xa0, v2
	v_add_u32_e32 v2, 0xb0, v2
	s_add_u32 s11, s54, s8
	v_ashrrev_i32_e32 v7, 31, v6
	v_ashrrev_i32_e32 v9, 31, v8
	v_ashrrev_i32_e32 v11, 31, v10
	v_ashrrev_i32_e32 v3, 31, v2
	s_addc_u32 s41, s55, s9
	s_lshl_b32 s8, s40, 8
	v_lshl_add_u64 v[6:7], v[6:7], 2, s[12:13]
	v_lshl_add_u64 v[8:9], v[8:9], 2, s[12:13]
	v_lshl_add_u64 v[10:11], v[10:11], 2, s[12:13]
	v_lshl_add_u64 v[2:3], v[2:3], 2, s[12:13]
	global_load_dword v146, v[4:5], off
	global_load_dword v170, v[4:5], off offset:64
	global_load_dword v169, v[4:5], off offset:128
	global_load_dword v168, v[4:5], off offset:192
	global_load_dword v167, v[6:7], off
	global_load_dword v166, v[8:9], off
	global_load_dword v165, v[10:11], off
	global_load_dword v1, v[2:3], off
	s_ashr_i32 s9, s8, 31
	s_lshl_b64 s[8:9], s[8:9], 1
	s_add_u32 s8, s11, s8
	s_addc_u32 s9, s41, s9
	s_lshl_b32 s10, s10, 1
	s_add_u32 s8, s8, s10
	s_addc_u32 s9, s9, 0
	v_and_b32_e32 v2, 48, v12
	global_load_dwordx4 v[6:9], v2, s[8:9]
	s_nop 0
	global_load_dwordx4 v[2:5], v2, s[8:9] offset:64
	s_andn2_b64 vcc, exec, s[14:15]
	s_cbranch_vccnz .LBB0_3417
	s_barrier
	s_branch .LBB0_3417
